# mLSTM chain: gain table in LDS + pipelined V-fragment reads in S2 + output-gate rows loaded one chunk ahead
# speedup vs baseline: 1.0043x; 1.0043x over previous
; #define GAS __attribute__((address_space(1)))
; __device__ __forceinline__ void p2_mlstm_chain(Frame& F, const Args& A, int ch) {
;     ...
;       if (tid < 64) ns[tid] = 0.f;
;       __syncthreads(); }
;     f32x4 Cst[4]; f32x4 Nst = (f32x4){0.f, 0.f, 0.f, 0.f};
; #pragma unroll
;     for (int i = 0; i < 4; ++i) Cst[i] = (f32x4){0.f, 0.f, 0.f, 0.f};
;     u32x4 qreg[2], kreg[2], vreg[4];
;     { const size_t tg0 = (size_t)b * SEQ;
; #pragma unroll
;       for (int j = 0; j < 2; ++j) { const int idx = tid + 512 * j, row = idx >> 3, part = idx & 7; const bf16* src = proj + (tg0 + row) * NP + h * 64 + part * 8; qreg[j] = *(const GAS u32x4*)src; kreg[j] = *(const GAS u32x4*)(src + 256); }
; #pragma unroll
;       for (int j = 0; j < 4; ++j) { const int idx = tid + 512 * j, row = idx >> 4, part = idx & 15; vreg[j] = *(const GAS u32x4*)(proj + (tg0 + row) * NP + 512 + h * 128 + part * 8); } }
.LBB0_374:
	v_writelane_b32 v254, s72, 8
	s_nop 1
	v_writelane_b32 v254, s73, 9
	s_or_b64 exec, exec, s[4:5]
	v_cmp_gt_i32_e64 s[2:3], 64, v48
	s_and_saveexec_b64 s[4:5], s[2:3]
	v_add_u32_e32 v2, 0x14800, v2
	v_mov_b32_e32 v3, 0
	ds_write_b32 v2, v3
	s_or_b64 exec, exec, s[4:5]
	s_lshl_b32 s60, s45, 7
	s_lshl_b32 s2, s45, 9
	s_add_u32 s4, s26, s2
	s_addc_u32 s5, s27, 0
	s_lshl_b64 s[2:3], s[42:43], 11
	s_add_u32 s6, s12, s60
	s_addc_u32 s7, s13, 0
	s_cmp_lt_u32 s68, 64
	s_cselect_b64 s[24:25], -1, 0
	s_cmp_gt_u32 s68, 63
	s_cselect_b64 s[26:27], -1, 0
	s_cmpk_gt_u32 s68, 0xbf
	s_cselect_b64 s[28:29], -1, 0
	s_cmpk_gt_u32 s68, 0x13f
	s_cselect_b64 s[30:31], -1, 0
	s_cmpk_gt_u32 s68, 0x1bf
	v_ashrrev_i32_e32 v38, 4, v48
	s_cselect_b64 s[82:83], -1, 0
	s_cmp_eq_u32 s93, 1
	v_lshlrev_b32_e32 v50, 4, v48
	v_ashrrev_i32_e32 v39, 31, v38
	s_cselect_b64 s[34:35], -1, 0
	s_cmp_eq_u32 s93, 2
	v_and_b32_e32 v106, 0x70, v50
	v_mov_b32_e32 v107, 0
	s_movk_i32 s46, 0x1400
	v_lshl_add_u64 v[20:21], s[2:3], 0, v[38:39]
	v_mov_b64_e32 v[28:29], s[12:13]
	v_ashrrev_i32_e32 v40, 4, v18
	v_ashrrev_i32_e32 v42, 4, v1
	v_ashrrev_i32_e32 v44, 4, v26
	v_lshrrev_b32_e32 v52, 4, v49
	s_cselect_b64 s[36:37], -1, 0
	s_cmp_eq_u32 s93, 3
	v_lshl_add_u64 v[10:11], s[6:7], 0, v[106:107]
	v_ashrrev_i32_e32 v34, 3, v48
	v_ashrrev_i32_e32 v36, 3, v18
	v_mad_u64_u32 v[22:23], s[6:7], v20, s46, v[28:29]
	v_ashrrev_i32_e32 v41, 31, v40
	v_ashrrev_i32_e32 v43, 31, v42
	v_ashrrev_i32_e32 v45, 31, v44
	s_mov_b32 s23, 0
	s_cselect_b64 s[38:39], -1, 0
	v_lshlrev_b32_e32 v53, 3, v48
	v_ashrrev_i32_e32 v35, 31, v34
	v_ashrrev_i32_e32 v37, 31, v36
	v_mad_i32_i24 v23, v21, s46, v23
	s_lshl_b32 s22, s45, 8
	v_lshl_add_u64 v[18:19], s[2:3], 0, v[40:41]
	v_lshl_add_u64 v[30:31], s[2:3], 0, v[42:43]
	v_lshl_add_u64 v[26:27], s[2:3], 0, v[44:45]
	v_lshlrev_b32_e32 v68, 2, v52
	v_lshlrev_b32_e32 v146, 5, v52
	v_lshlrev_b32_e32 v39, 3, v52
	v_lshlrev_b32_e32 v52, 1, v52
	v_lshl_add_u64 v[2:3], s[2:3], 0, v[34:35]
	v_lshl_add_u64 v[12:13], s[2:3], 0, v[36:37]
	v_lshl_add_u64 v[20:21], v[22:23], 0, s[22:23]
	v_mad_u64_u32 v[22:23], s[6:7], v18, s46, v[28:29]
	v_mad_u64_u32 v[32:33], s[6:7], v30, s46, v[28:29]
	v_mad_u64_u32 v[28:29], s[2:3], v26, s46, v[28:29]
	v_lshrrev_b32_e32 v37, 1, v48
	v_bfe_u32 v70, v48, 2, 2
	v_and_b32_e32 v43, 24, v53
	v_xor_b32_e32 v53, v52, v68
	v_mad_i32_i24 v23, v19, s46, v23
	v_mad_i32_i24 v33, v31, s46, v33
	v_mad_i32_i24 v29, v27, s46, v29
	v_and_or_b32 v74, v53, 4, v70
	v_and_b32_e32 v77, 2, v52
	v_and_b32_e32 v52, 3, v48
	v_bitop3_b32 v37, v37, 4, v48 bitop3:0x48
	v_lshrrev_b32_e32 v53, 2, v34
	v_and_b32_e32 v64, 15, v48
	v_and_b32_e32 v106, 0xf0, v50
	v_lshl_add_u64 v[18:19], v[22:23], 0, s[22:23]
	v_lshl_add_u64 v[30:31], v[32:33], 0, s[22:23]
	v_lshl_add_u64 v[26:27], v[28:29], 0, s[22:23]
	v_bfe_u32 v35, v48, 1, 2
	v_bitop3_b32 v37, v37, s93, v52 bitop3:0x36
	v_bfe_u32 v52, v34, 1, 1
	v_and_b32_e32 v53, 2, v53
	v_lshrrev_b32_e32 v59, 2, v36
	v_lshl_add_u64 v[20:21], v[20:21], 0, v[106:107]
	v_lshl_add_u64 v[22:23], v[18:19], 0, v[106:107]
	v_lshl_add_u64 v[30:31], v[30:31], 0, v[106:107]
	v_lshl_add_u64 v[32:33], v[26:27], 0, v[106:107]
	v_lshrrev_b32_e32 v58, 5, v49
	s_add_i32 s8, 0, 0x10800
	v_and_b32_e32 v106, 48, v49
	v_lshlrev_b32_e32 v49, 8, v64
	v_lshlrev_b32_e32 v37, 5, v37
	v_bitop3_b32 v52, v52, v35, v53 bitop3:0x36
	v_bfe_u32 v57, v36, 1, 1
	v_and_b32_e32 v59, 2, v59
	v_add3_u32 v49, s8, v49, v37
	v_lshlrev_b32_e32 v37, 7, v34
	v_lshlrev_b32_e32 v52, 5, v52
	v_bitop3_b32 v35, v57, v35, v59 bitop3:0x36
	v_add3_u32 v52, 0, v37, v52
	v_lshlrev_b32_e32 v37, 7, v36
	v_lshlrev_b32_e32 v35, 5, v35
	v_lshrrev_b32_e32 v59, 1, v38
	v_bfe_u32 v55, v48, 1, 3
	v_add3_u32 v57, 0, v37, v35
	v_and_b32_e32 v37, 3, v38
	v_bitop3_b32 v59, v59, 4, v38 bitop3:0x48
	v_mad_u64_u32 v[6:7], s[6:7], v2, s46, v[10:11]
	v_mad_u64_u32 v[14:15], s[6:7], v12, s46, v[10:11]
	v_bitop3_b32 v37, v59, v55, v37 bitop3:0x36
	v_mad_i32_i24 v7, v3, s46, v7
	v_mad_i32_i24 v15, v13, s46, v15
	v_lshlrev_b32_e32 v35, 8, v38
	v_lshlrev_b32_e32 v37, 5, v37
	v_lshrrev_b32_e32 v60, 1, v40
	s_waitcnt lgkmcnt(0)
	s_barrier
	global_load_dwordx4 v[2:5], v[6:7], off
	s_nop 0
	global_load_dwordx4 v[6:9], v[6:7], off offset:512
	s_nop 0
	global_load_dwordx4 v[10:13], v[14:15], off
	s_nop 0
	global_load_dwordx4 v[14:17], v[14:15], off offset:512
	s_nop 0
	global_load_dwordx4 v[18:21], v[20:21], off offset:1024
	s_nop 0
	global_load_dwordx4 v[22:25], v[22:23], off offset:1024
	s_nop 0
	global_load_dwordx4 v[26:29], v[30:31], off offset:1024
	s_nop 0
	global_load_dwordx4 v[30:33], v[32:33], off offset:1024
	v_add3_u32 v59, 0, v35, v37
	v_and_b32_e32 v37, 3, v40
	v_bitop3_b32 v60, v60, 4, v40 bitop3:0x48
	v_bitop3_b32 v37, v60, v55, v37 bitop3:0x36
	v_lshlrev_b32_e32 v35, 8, v40
	v_lshlrev_b32_e32 v37, 5, v37
	v_lshrrev_b32_e32 v61, 1, v42
	v_add3_u32 v60, 0, v35, v37
	v_and_b32_e32 v37, 3, v42
	v_bitop3_b32 v61, v61, 4, v42 bitop3:0x48
	v_bitop3_b32 v37, v61, v55, v37 bitop3:0x36
	v_lshlrev_b32_e32 v35, 8, v42
	v_lshlrev_b32_e32 v37, 5, v37
	v_lshrrev_b32_e32 v62, 1, v44
	v_or_b32_e32 v54, s44, v64
	v_and_b32_e32 v1, 7, v48
	s_movk_i32 s6, 0x90
	v_add3_u32 v61, 0, v35, v37
	v_and_b32_e32 v37, 3, v44
	v_bitop3_b32 v62, v62, 4, v44 bitop3:0x48
	v_lshlrev_b32_e32 v63, 4, v1
	v_mul_lo_u32 v1, v54, s6
	v_bitop3_b32 v37, v62, v55, v37 bitop3:0x36
	v_and_b32_e32 v41, 16, v50
	v_add_u32_e32 v50, 0, v1
	v_lshrrev_b32_e32 v1, 2, v48
	v_lshlrev_b32_e32 v35, 8, v44
	v_lshlrev_b32_e32 v37, 5, v37
	v_bfe_u32 v56, v48, 1, 1
	v_and_b32_e32 v66, 2, v1
	v_and_b32_e32 v69, 16, v48
	v_add3_u32 v62, 0, v35, v37
; __device__ __forceinline__ void p2_mlstm_chain(Frame& F, const Args& A, int ch) {
;     ...
;         const size_t tg0 = (size_t)b * SEQ + c * 128; const int t = 16 * w + tl;
; #pragma unroll
;         for (int j = 0; j < 2; ++j) { const int idx = tid + 512 * j, row = idx >> 3, part = idx & 7; *(LAS u32x4*)(L + ML_QS + row * 144 + part * 16) = qreg[j];
;             *(LAS u32x4*)(L + ML_KS + 128 * row + 32 * ((part >> 1) ^ swzg(row)) + 16 * (part & 1)) = kreg[j]; }
; #pragma unroll
;         for (int j = 0; j < 4; ++j) { const int idx = tid + 512 * j, row = idx >> 4, part = idx & 15; *(LAS u32x4*)(L + ML_VS + 256 * row + 32 * ((part >> 1) ^ swzf(row)) + 16 * (part & 1)) = vreg[j]; }
;         const float mc = sMC[c], Mn = sMC[32 + c], Mt = sM[c * 128 + t], lf = sLF[c * 128 + t];
;         if (tid < 128) sWK[tid] = __builtin_amdgcn_exp2f((sA[c * 128 + tid] - Mn) * 1.4426950408889634f);
;         __syncthreads();
;         if (c < 15) { const size_t tn = tg0 + 128;
; #pragma unroll
;             for (int j = 0; j < 2; ++j) { const int idx = tid + 512 * j, row = idx >> 3, part = idx & 7; const bf16* src = proj + (tn + row) * NP + h * 64 + part * 8; qreg[j] = *(const GAS u32x4*)src; kreg[j] = *(const GAS u32x4*)(src + 256); }
; #pragma unroll
;             for (int j = 0; j < 4; ++j) { const int idx = tid + 512 * j, row = idx >> 4, part = idx & 15; vreg[j] = *(const GAS u32x4*)(proj + (tn + row) * NP + 512 + h * 128 + part * 8); } }
;         u32x2 og[8];
; #pragma unroll
;         for (int vb = 0; vb < 8; ++vb) og[vb] = *(const GAS u32x2*)(proj + (tg0 + t) * NP + 1024 + h * 128 + 16 * vb + 4 * fq);
;         bf16x8 qf[2];
; #pragma unroll
;         for (int ds = 0; ds < 2; ++ds) qf[ds] = *(const LAS bf16x8*)(L + ML_QS + t * 144 + ds * 64 + fq * 16);
;         unsigned sfr[4][4];
; #pragma unroll
;         for (int i = 0; i < 4; ++i)
; #pragma unroll
;             for (int j = 0; j < 4; ++j) sfr[i][j] = 0u;
;         float den = 0.f;
; #pragma unroll
;         for (int sb = 0; sb < 8; ++sb) {
;             if (sb <= w) {
;                 f32x4 G = (f32x4){0.f, 0.f, 0.f, 0.f}; const int sr = 16 * sb + tl;
; #pragma unroll
;                 for (int ds = 0; ds < 2; ++ds) { const bf16x8 a = *(const LAS bf16x8*)(L + ML_KS + 128 * sr + 32 * ((2 * ds + (fq >> 1)) ^ swzg(sr)) + 16 * (fq & 1)); G = __builtin_amdgcn_mfma_f32_16x16x32_bf16(a, qf[ds], G, 0, 0, 0); }
	v_lshlrev_b32_e32 v35, 7, v64
	v_or_b32_e32 v67, v56, v66
	v_add3_u32 v55, 0, v69, v35
	v_bitop3_b32 v35, v56, v58, v66 bitop3:0x36
	v_lshlrev_b32_e32 v56, 5, v35
	v_bitop3_b32 v35, v58, v67, 2 bitop3:0x36
	v_lshlrev_b32_e32 v58, 5, v35
	v_or_b32_e32 v35, 3, v68
	v_cmp_gt_u32_e64 s[10:11], v35, v54
	v_or_b32_e32 v35, 17, v68
	v_or_b32_e32 v37, 2, v68
	v_cmp_gt_u32_e64 s[48:49], v35, v54
	v_cmp_gt_u32_e64 s[12:13], v37, v54
	v_or_b32_e32 v37, 16, v68
	v_writelane_b32 v254, s48, 10
	v_or_b32_e32 v35, 19, v68
	v_xor_b32_e32 v66, 16, v46
	v_writelane_b32 v254, s49, 11
	v_cmp_gt_u32_e64 s[48:49], v37, v54
	v_or_b32_e32 v37, 18, v68
	v_add_u32_e32 v47, 64, v47
	v_writelane_b32 v254, s48, 12
	s_and_b64 s[40:41], s[40:41], vcc
	v_cmp_lt_i32_e32 vcc, v66, v47
	v_writelane_b32 v254, s49, 13
	v_cmp_gt_u32_e64 s[48:49], v35, v54
	v_or_b32_e32 v35, 33, v68
	v_cndmask_b32_e32 v69, v46, v66, vcc
	v_writelane_b32 v254, s48, 14
	v_xor_b32_e32 v66, 32, v46
	v_cmp_lt_i32_e32 vcc, v66, v47
	v_writelane_b32 v254, s49, 15
	v_cmp_gt_u32_e64 s[48:49], v37, v54
	v_or_b32_e32 v37, 32, v68
	v_cndmask_b32_e32 v79, v46, v66, vcc
	v_writelane_b32 v254, s48, 16
	v_add_u32_e32 v46, s44, v64
	v_mov_b32_e32 v47, v107
	v_writelane_b32 v254, s49, 17
	v_cmp_gt_u32_e64 s[48:49], v35, v54
	v_or_b32_e32 v35, 35, v68
	v_and_b32_e32 v51, 48, v48
	v_writelane_b32 v254, s48, 18
	v_lshlrev_b64 v[66:67], 11, v[46:47]
	v_lshrrev_b32_e32 v81, 1, v51
	v_writelane_b32 v254, s49, 19
	v_cmp_gt_u32_e64 s[48:49], v37, v54
	v_or_b32_e32 v37, 34, v68
	s_mov_b64 s[44:45], 0x5000080
	v_writelane_b32 v254, s48, 20
	v_mov_b32_e32 v80, 0xa00000
	v_or_b32_e32 v76, 4, v70
	v_writelane_b32 v254, s49, 21
	v_cmp_gt_u32_e64 s[48:49], v35, v54
	v_or_b32_e32 v35, 49, v68
	v_or_b32_e32 v87, v39, v76
	v_writelane_b32 v254, s48, 22
	v_lshrrev_b32_e32 v89, 1, v87
	v_and_b32_e32 v90, 4, v89
	v_writelane_b32 v254, s49, 23
	v_cmp_gt_u32_e64 s[48:49], v37, v54
	v_or_b32_e32 v37, 48, v68
	v_bitop3_b32 v90, v90, s93, v70 bitop3:0x36
	v_writelane_b32 v254, s48, 24
	v_lshlrev_b32_e32 v90, 5, v90
	v_lshlrev_b32_e32 v88, 8, v87
	v_writelane_b32 v254, s49, 25
	v_cmp_gt_u32_e64 s[48:49], v35, v54
	v_or_b32_e32 v35, 51, v68
	v_xor_b32_e32 v90, 0x80, v90
	v_writelane_b32 v254, s48, 26
	v_add3_u32 v88, 0, v90, v88
	v_and_b32_e32 v71, 4, v68
	v_writelane_b32 v254, s49, 27
	v_cmp_gt_u32_e64 s[48:49], v37, v54
	v_or_b32_e32 v37, 50, v68
	v_or_b32_e32 v72, v71, v70
	v_writelane_b32 v254, s48, 28
	s_movk_i32 s22, 0x80
	v_add_u32_e32 v73, s8, v43
	v_writelane_b32 v254, s49, 29
	v_cmp_gt_u32_e64 s[48:49], v35, v54
	v_or_b32_e32 v35, 0x41, v68
	v_cmp_gt_i32_e64 s[2:3], s22, v48
	v_writelane_b32 v254, s48, 30
	v_lshlrev_b32_e32 v65, 2, v48
	v_lshrrev_b32_e32 v78, 3, v48
	v_writelane_b32 v254, s49, 31
	v_cmp_gt_u32_e64 s[48:49], v37, v54
	v_or_b32_e32 v37, 64, v68
	v_mul_lo_u32 v48, v34, s6
	v_writelane_b32 v254, s48, 32
	v_mul_lo_u32 v53, v36, s6
	v_bitop3_b32 v71, v71, s93, v70 bitop3:0x36
	v_writelane_b32 v254, s49, 33
	v_cmp_gt_u32_e64 s[48:49], v35, v54
	v_or_b32_e32 v35, 0x43, v68
	v_add_u32_e32 v75, 0, v43
	v_writelane_b32 v254, s48, 34
	v_lshl_add_u32 v71, v71, 5, 0
	s_add_i32 s7, 0, 0x14a00
	v_writelane_b32 v254, s49, 35
	v_cmp_gt_u32_e64 s[48:49], v37, v54
	v_or_b32_e32 v37, 0x42, v68
	v_and_or_b32 v78, v78, 1, v77
	v_writelane_b32 v254, s48, 36
	v_add_u32_e32 v1, s7, v65
	v_add_u32_e32 v147, s7, v146
	v_writelane_b32 v254, s49, 37
	s_lshl_b64 s[48:49], s[42:43], 22
	s_lshl_b32 s43, s33, 8
	v_lshl_add_u64 v[66:67], s[48:49], 0, v[66:67]
	s_and_b32 s50, s43, 0x300
	v_or3_b32 v66, v66, s50, v81
	v_lshl_add_u64 v[66:67], s[58:59], 0, v[66:67]
	v_lshl_add_u64 v[110:111], v[66:67], 0, s[44:45]
	v_mad_i64_i32 v[66:67], s[44:45], v38, s46, 0
	v_mad_i64_i32 v[66:67], s[44:45], s42, v80, v[66:67]
	v_lshlrev_b32_e32 v38, 4, v64
	v_or3_b32 v66, v66, s50, v38
	v_lshl_add_u64 v[66:67], s[58:59], 0, v[66:67]
	s_mov_b64 s[44:45], 0x270a0400
	v_lshl_add_u64 v[112:113], v[66:67], 0, s[44:45]
	v_mad_i64_i32 v[66:67], s[48:49], v40, s46, 0
	v_mad_i64_i32 v[66:67], s[48:49], s42, v80, v[66:67]
	v_or3_b32 v66, v66, s50, v38
	v_lshl_add_u64 v[66:67], s[58:59], 0, v[66:67]
	v_lshl_add_u64 v[114:115], v[66:67], 0, s[44:45]
	v_mad_i64_i32 v[66:67], s[48:49], v42, s46, 0
	v_mad_i64_i32 v[66:67], s[48:49], s42, v80, v[66:67]
	v_or3_b32 v66, v66, s50, v38
	v_lshl_add_u64 v[66:67], s[58:59], 0, v[66:67]
	v_or_b32_e32 v42, 32, v39
	v_lshl_add_u64 v[116:117], v[66:67], 0, s[44:45]
	v_mad_i64_i32 v[66:67], s[48:49], v44, s46, 0
	v_or_b32_e32 v44, v42, v70
	v_or_b32_e32 v42, v42, v76
	v_lshrrev_b32_e32 v91, 1, v42
	v_and_b32_e32 v92, 4, v91
	v_bitop3_b32 v92, v92, s93, v70 bitop3:0x36
	v_lshlrev_b32_e32 v92, 5, v92
	v_lshlrev_b32_e32 v90, 8, v42
	v_xor_b32_e32 v92, 0x80, v92
	v_add3_u32 v90, 0, v92, v90
	v_or_b32_e32 v92, 64, v39
	v_or_b32_e32 v93, v92, v70
	v_or_b32_e32 v92, v92, v76
	v_lshrrev_b32_e32 v96, 1, v92
	v_and_b32_e32 v97, 4, v96
	v_mad_i64_i32 v[66:67], s[48:49], s42, v80, v[66:67]
	v_bitop3_b32 v97, v97, s93, v70 bitop3:0x36
	v_or3_b32 v66, v66, s50, v38
	v_or_b32_e32 v38, 0x51, v68
	v_lshlrev_b32_e32 v97, 5, v97
	v_lshl_add_u64 v[66:67], s[58:59], 0, v[66:67]
	v_cmp_gt_u32_e64 s[48:49], v38, v54
	v_lshlrev_b32_e32 v38, 5, v72
	v_lshlrev_b32_e32 v95, 8, v92
	v_xor_b32_e32 v97, 0x80, v97
	v_lshl_add_u64 v[118:119], v[66:67], 0, s[44:45]
	v_cmp_gt_u32_e64 s[44:45], v35, v54
	v_xad_u32 v149, v38, s22, v73
	s_movk_i32 s22, 0xa0
	v_add3_u32 v95, 0, v97, v95
	v_or_b32_e32 v97, 0x60, v39
	v_writelane_b32 v254, s44, 38
	v_xad_u32 v150, v38, s22, v73
	s_movk_i32 s22, 0xc0
	v_or_b32_e32 v76, v97, v76
	v_writelane_b32 v254, s45, 39
; __device__ __forceinline__ void p2_mlstm_chain(Frame& F, const Args& A, int ch) {
;     ...
; #pragma unroll
;         for (int j = 0; j < 2; ++j) { const int idx = tid + 512 * j, row = idx >> 3, part = idx & 7; *(LAS u32x4*)(L + ML_QS + row * 144 + part * 16) = qreg[j];
;             *(LAS u32x4*)(L + ML_KS + 128 * row + 32 * ((part >> 1) ^ swzg(row)) + 16 * (part & 1)) = kreg[j]; }
; #pragma unroll
;         for (int j = 0; j < 4; ++j) { const int idx = tid + 512 * j, row = idx >> 4, part = idx & 15; *(LAS u32x4*)(L + ML_VS + 256 * row + 32 * ((part >> 1) ^ swzf(row)) + 16 * (part & 1)) = vreg[j]; }
;         const float mc = sMC[c], Mn = sMC[32 + c], Mt = sM[c * 128 + t], lf = sLF[c * 128 + t];
;         if (tid < 128) sWK[tid] = __builtin_amdgcn_exp2f((sA[c * 128 + tid] - Mn) * 1.4426950408889634f);
;         __syncthreads();
;         if (c < 15) { const size_t tn = tg0 + 128;
; #pragma unroll
;             for (int j = 0; j < 2; ++j) { const int idx = tid + 512 * j, row = idx >> 3, part = idx & 7; const bf16* src = proj + (tn + row) * NP + h * 64 + part * 8; qreg[j] = *(const GAS u32x4*)src; kreg[j] = *(const GAS u32x4*)(src + 256); }
; #pragma unroll
;             for (int j = 0; j < 4; ++j) { const int idx = tid + 512 * j, row = idx >> 4, part = idx & 15; vreg[j] = *(const GAS u32x4*)(proj + (tn + row) * NP + 512 + h * 128 + part * 8); } }
;         u32x2 og[8];
; #pragma unroll
;         for (int vb = 0; vb < 8; ++vb) og[vb] = *(const GAS u32x2*)(proj + (tg0 + t) * NP + 1024 + h * 128 + 16 * vb + 4 * fq);
;         bf16x8 qf[2];
; #pragma unroll
;         for (int ds = 0; ds < 2; ++ds) qf[ds] = *(const LAS bf16x8*)(L + ML_QS + t * 144 + ds * 64 + fq * 16);
;         unsigned sfr[4][4];
; #pragma unroll
;         for (int i = 0; i < 4; ++i)
; #pragma unroll
;             for (int j = 0; j < 4; ++j) sfr[i][j] = 0u;
;         float den = 0.f;
; #pragma unroll
;         for (int sb = 0; sb < 8; ++sb) {
;             if (sb <= w) {
;                 f32x4 G = (f32x4){0.f, 0.f, 0.f, 0.f}; const int sr = 16 * sb + tl;
; #pragma unroll
;                 for (int ds = 0; ds < 2; ++ds) { const bf16x8 a = *(const LAS bf16x8*)(L + ML_KS + 128 * sr + 32 * ((2 * ds + (fq >> 1)) ^ swzg(sr)) + 16 * (fq & 1)); G = __builtin_amdgcn_mfma_f32_16x16x32_bf16(a, qf[ds], G, 0, 0, 0); }
;                 const f32x4 as = *(const LAS f32x4*)(sA + c * 128 + 16 * sb + 4 * fq);
	v_mad_i64_i32 v[34:35], s[44:45], v34, s46, 0
	v_mad_i64_i32 v[66:67], s[44:45], v36, s46, 0
	v_mad_u64_u32 v[46:47], s[44:45], v46, s46, 0
	v_xad_u32 v151, v38, s22, v73
	s_movk_i32 s22, 0x60
	v_lshrrev_b32_e32 v99, 1, v76
	v_cmp_gt_u32_e64 s[46:47], v37, v54
	v_or_b32_e32 v40, 0x50, v68
	v_mad_i64_i32 v[36:37], s[44:45], s42, v80, v[34:35]
	v_mad_i64_i32 v[34:35], s[44:45], s42, v80, v[66:67]
	v_mad_i64_i32 v[46:47], s[42:43], s42, v80, v[46:47]
	v_xad_u32 v152, v38, s22, v73
	s_movk_i32 s22, 0xe0
	v_and_b32_e32 v100, 4, v99
	v_xad_u32 v153, v38, s22, v73
	v_or3_b32 v46, v46, s50, v81
	v_cmp_gt_u32_e64 s[50:51], v40, v54
	v_or_b32_e32 v40, v39, v70
	v_add_u32_e32 v157, v73, v38
	v_xad_u32 v159, v38, 32, v73
	v_xad_u32 v160, v38, 64, v73
	v_or_b32_e32 v38, v68, v70
	v_or_b32_e32 v98, v97, v70
	v_bitop3_b32 v70, v100, s93, v70 bitop3:0x36
	v_lshlrev_b32_e32 v156, 8, v40
	v_lshlrev_b32_e32 v158, 8, v44
	v_lshl_add_u32 v163, v40, 7, v75
	v_and_or_b32 v40, v89, 1, v77
	v_lshl_add_u32 v170, v44, 7, v75
	v_and_or_b32 v44, v91, 1, v77
	v_lshl_add_u32 v94, v93, 8, v71
	v_lshl_add_u32 v173, v93, 7, v75
	v_and_or_b32 v93, v96, 1, v77
	v_lshlrev_b32_e32 v70, 5, v70
	v_and_or_b32 v77, v99, 1, v77
	s_add_i32 s7, 0, 0x14800
	v_lshl_add_u64 v[46:47], s[58:59], 0, v[46:47]
	s_mov_b64 s[42:43], 0x27000880
	v_lshlrev_b32_e32 v162, 5, v74
	v_lshlrev_b32_e32 v166, 5, v40
	v_lshlrev_b32_e32 v172, 5, v44
	v_lshlrev_b32_e32 v175, 5, v93
	v_lshlrev_b32_e32 v97, 8, v76
	v_xor_b32_e32 v70, 0x80, v70
	v_lshlrev_b32_e32 v178, 5, v77
	v_add_u32_e32 v45, 0, v63
	v_lshrrev_b32_e32 v233, 7, v0
	v_cmp_eq_u32_e64 s[98:99], 0, v233
	s_and_saveexec_b64 s[100:101], s[98:99]
	v_lshlrev_b32_e32 v232, 2, v0
	global_load_dword v233, v232, s[4:5]
	v_add_u32_e32 v232, 0x1c000, v232
	s_waitcnt vmcnt(0)
	ds_write_b32 v232, v233
	s_or_b64 exec, exec, s[100:101]
	v_bfe_u32 v252, v0, 4, 2
	v_lshlrev_b32_e32 v252, 4, v252
	v_add_u32_e32 v252, 0x1c000, v252
	v_lshl_add_u64 v[108:109], s[4:5], 0, v[106:107]
	v_cmp_eq_u32_e64 s[4:5], 0, v64
	v_lshl_add_u32 v148, v54, 2, s7
	v_cmp_gt_u32_e64 s[6:7], v68, v54
	v_cmp_lt_u32_e64 s[8:9], v68, v54
	v_lshl_add_u64 v[120:121], v[46:47], 0, s[42:43]
	v_or_b32_e32 v66, 0x53, v68
	v_or_b32_e32 v67, 0x52, v68
	v_or_b32_e32 v72, 0x61, v68
	v_or_b32_e32 v80, 0x60, v68
	v_or_b32_e32 v81, 0x63, v68
	v_or_b32_e32 v82, 0x62, v68
	v_or_b32_e32 v83, 0x71, v68
	v_or_b32_e32 v84, 0x70, v68
	v_or_b32_e32 v85, 0x73, v68
	v_or_b32_e32 v86, 0x72, v68
	v_lshlrev_b32_e32 v154, 2, v69
	v_lshlrev_b32_e32 v155, 2, v79
	v_lshl_add_u32 v161, v38, 8, v75
	v_xor_b32_e32 v38, 32, v162
	v_xor_b32_e32 v46, 64, v162
	v_xor_b32_e32 v47, 0x60, v162
	v_xor_b32_e32 v68, 0x80, v162
	v_xor_b32_e32 v69, 0xa0, v162
	v_xor_b32_e32 v73, 0xc0, v162
	v_xor_b32_e32 v74, 0xe0, v162
	v_add_u32_e32 v79, v71, v156
	v_lshl_add_u32 v164, v87, 7, v75
	v_lshlrev_b32_e32 v165, 5, v78
	v_xor_b32_e32 v40, 32, v166
	v_xor_b32_e32 v78, 64, v166
	v_xor_b32_e32 v87, 0x60, v166
	v_add_u32_e32 v89, v71, v158
	v_lshl_add_u32 v171, v42, 7, v75
	v_xor_b32_e32 v42, 32, v172
	v_xor_b32_e32 v44, 64, v172
	v_xor_b32_e32 v91, 0x60, v172
	v_lshl_add_u32 v174, v92, 7, v75
	v_xor_b32_e32 v92, 32, v175
	v_xor_b32_e32 v93, 64, v175
	v_xor_b32_e32 v96, 0x60, v175
	v_lshl_add_u32 v71, v98, 8, v71
	v_add3_u32 v70, 0, v70, v97
	v_lshl_add_u32 v176, v98, 7, v75
	v_lshl_add_u32 v177, v76, 7, v75
	v_xor_b32_e32 v75, 32, v178
	v_xor_b32_e32 v76, 64, v178
	v_xor_b32_e32 v77, 0x60, v178
	v_lshlrev_b32_e32 v64, 2, v64
	v_or3_b32 v36, v36, s60, v63
	v_or3_b32 v34, v34, s60, v63
	v_xor_b32_e32 v167, 32, v165
	v_xor_b32_e32 v168, 64, v165
	v_xor_b32_e32 v169, 0x60, v165
	v_add_u32_e32 v179, 0x15000, v65
	v_lshl_or_b32 v180, s93, 6, v64
	v_lshl_add_u64 v[122:123], s[58:59], 0, v[36:37]
	v_lshl_add_u64 v[124:125], s[58:59], 0, v[34:35]
	v_mov_b32_e32 v34, v107
	v_mov_b32_e32 v35, v107
	v_mov_b32_e32 v36, v107
	v_mov_b32_e32 v37, v107
	v_add_u32_e32 v181, v45, v48
	v_add_u32_e32 v182, v52, v41
	v_add_u32_e32 v183, v45, v53
	v_add_u32_e32 v184, v57, v41
	v_add_u32_e32 v185, v59, v41
	v_add_u32_e32 v186, v60, v41
	v_add_u32_e32 v187, v61, v41
	v_add_u32_e32 v188, v62, v41
	v_add_u32_e32 v189, v50, v51
	v_mov_b32_e32 v190, 0x358637bd
	v_add_u32_e32 v191, v79, v43
	v_add_u32_e32 v192, v88, v43
	v_add_u32_e32 v193, v164, v40
	v_add_u32_e32 v194, v164, v78
	v_add_u32_e32 v195, v164, v87
	v_add_u32_e32 v196, v89, v43
	v_add_u32_e32 v197, v90, v43
	v_add_u32_e32 v198, v171, v42
	v_add_u32_e32 v199, v171, v44
	v_add_u32_e32 v200, v171, v91
	v_add_u32_e32 v201, v94, v43
	v_add_u32_e32 v202, v95, v43
	v_add_u32_e32 v203, v174, v92
	v_add_u32_e32 v204, v174, v93
	v_add_u32_e32 v205, v174, v96
	v_add_u32_e32 v206, v71, v43
	v_add_u32_e32 v207, v70, v43
	v_add_u32_e32 v208, v177, v75
	v_add_u32_e32 v209, v177, v76
	v_add_u32_e32 v210, v177, v77
	v_add_u32_e32 v211, v49, v39
	v_add_u32_e32 v212, v55, v56
	v_add_u32_e32 v213, v55, v58
	v_add_u32_e32 v214, v161, v38
	v_add_u32_e32 v215, v161, v46
	v_add_u32_e32 v216, v161, v47
	v_add_u32_e32 v217, v161, v68
	v_add_u32_e32 v218, v161, v69
	v_add_u32_e32 v219, v161, v73
	v_add_u32_e32 v220, v161, v74
	v_mov_b32_e32 v50, v107
	v_mov_b32_e32 v51, v107
	v_mov_b32_e32 v52, v107
	v_mov_b32_e32 v53, v107
	v_mov_b32_e32 v46, v107
	v_mov_b32_e32 v47, v107
	v_mov_b32_e32 v48, v107
	v_mov_b32_e32 v49, v107
	v_mov_b32_e32 v42, v107
	v_mov_b32_e32 v43, v107
	v_mov_b32_e32 v44, v107
	v_mov_b32_e32 v45, v107
	v_mov_b32_e32 v38, v107
	v_mov_b32_e32 v39, v107
	v_mov_b32_e32 v40, v107
	v_mov_b32_e32 v41, v107
	v_cmp_gt_u32_e64 s[86:87], v66, v54
	v_cmp_gt_u32_e64 s[90:91], v67, v54
	v_cmp_gt_u32_e64 s[44:45], v72, v54
	v_cmp_gt_u32_e64 s[94:95], v80, v54
	v_cmp_gt_u32_e64 s[60:61], v81, v54
	v_cmp_gt_u32_e64 s[62:63], v82, v54
	v_cmp_gt_u32_e64 s[64:65], v83, v54
	v_cmp_gt_u32_e64 s[66:67], v84, v54
	v_cmp_gt_u32_e64 s[68:69], v85, v54
	v_cmp_gt_u32_e64 s[70:71], v86, v54
	s_mov_b64 s[42:43], 0
	s_mov_b32 s22, 0x3e000000
	global_load_dwordx2 v[140:141], v[120:121], off offset:-128
	global_load_dwordx2 v[138:139], v[120:121], off offset:-96
	global_load_dwordx2 v[136:137], v[120:121], off offset:-64
	global_load_dwordx2 v[134:135], v[120:121], off offset:-32
	global_load_dwordx2 v[132:133], v[120:121], off
	global_load_dwordx2 v[130:131], v[120:121], off offset:32
	global_load_dwordx2 v[128:129], v[120:121], off offset:64
	global_load_dwordx2 v[126:127], v[120:121], off offset:96
	s_branch .LBB0_378

; #define LAS __attribute__((address_space(3)))
; __device__ __forceinline__ int swzf(int r) { return (r & 3) | ((((r >> 2) ^ (r >> 3)) & 1) << 2); }
; __device__ __forceinline__ int swzg(int r) { return ((r >> 1) & 1) | (((r >> 3) & 1) << 1); }
; __device__ __forceinline__ void p2_mlstm_chain(Frame& F, const Args& A, int ch) {
;     ...
;     for (int c = 0; c < 16; ++c) {
;         const size_t tg0 = (size_t)b * SEQ + c * 128; const int t = 16 * w + tl;
; #pragma unroll
;         for (int j = 0; j < 2; ++j) { const int idx = tid + 512 * j, row = idx >> 3, part = idx & 7; *(LAS u32x4*)(L + ML_QS + row * 144 + part * 16) = qreg[j];
;             *(LAS u32x4*)(L + ML_KS + 128 * row + 32 * ((part >> 1) ^ swzg(row)) + 16 * (part & 1)) = kreg[j]; }
; #pragma unroll
;         for (int j = 0; j < 4; ++j) { const int idx = tid + 512 * j, row = idx >> 4, part = idx & 15; *(LAS u32x4*)(L + ML_VS + 256 * row + 32 * ((part >> 1) ^ swzf(row)) + 16 * (part & 1)) = vreg[j]; }
;         const float mc = sMC[c], Mn = sMC[32 + c], Mt = sM[c * 128 + t], lf = sLF[c * 128 + t];
;         if (tid < 128) sWK[tid] = __builtin_amdgcn_exp2f((sA[c * 128 + tid] - Mn) * 1.4426950408889634f);
.LBB0_378:
	s_add_i32 s72, s23, 0
	s_add_i32 s73, s72, 0x1b000
	s_waitcnt vmcnt(15)
	ds_write_b128 v181, v[2:5]
	s_waitcnt vmcnt(14)
	ds_write_b128 v182, v[6:9] offset:18432
	s_waitcnt vmcnt(13)
	ds_write_b128 v183, v[10:13]
	s_waitcnt vmcnt(12)
	ds_write_b128 v184, v[14:17] offset:18432
	s_waitcnt vmcnt(11)
	ds_write_b128 v185, v[18:21] offset:34816
	s_waitcnt vmcnt(10)
	ds_write_b128 v186, v[22:25] offset:34816
	s_waitcnt vmcnt(9)
	ds_write_b128 v187, v[26:29] offset:34816
	s_waitcnt vmcnt(8)
	ds_write_b128 v188, v[30:33] offset:34816
	v_mov_b32_e32 v54, s73
	s_add_i32 s72, s72, 0x1b080
	v_add_u32_e32 v56, 0, v180
	v_mov_b32_e32 v55, s72
	v_add_u32_e32 v57, 0x17000, v56
	v_add_u32_e32 v56, 0x19000, v56
	ds_read_b32 v107, v54
	ds_read_b32 v221, v55
	ds_read_b32 v78, v57
	ds_read_b32 v142, v56
	s_and_saveexec_b64 s[72:73], s[2:3]
	s_cbranch_execz .LBB0_380
	v_add_u32_e32 v54, 0, v179
	ds_read_b32 v54, v54
	s_waitcnt lgkmcnt(0)
	v_sub_f32_e32 v54, v54, v221
	v_mul_f32_e32 v54, 0x3fb8aa3b, v54
	v_exp_f32_e32 v54, v54
	ds_write_b32 v1, v54

; #define LAS __attribute__((address_space(3)))
; __device__ __forceinline__ unsigned cvt_pk_bf16(float lo, float hi) { unsigned r; asm volatile("v_cvt_pk_bf16_f32 %0, %1, %2" : "=v"(r) : "v"(lo), "v"(hi)); return r; }
; __device__ __forceinline__ int swzg(int r) { return ((r >> 1) & 1) | (((r >> 3) & 1) << 1); }
; __device__ __forceinline__ void p2_mlstm_chain(Frame& F, const Args& A, int ch) {
;     ...
;         for (int sb = 0; sb < 8; ++sb) {
;             if (sb <= w) {
;                 f32x4 G = (f32x4){0.f, 0.f, 0.f, 0.f}; const int sr = 16 * sb + tl;
; #pragma unroll
;                 for (int ds = 0; ds < 2; ++ds) { const bf16x8 a = *(const LAS bf16x8*)(L + ML_KS + 128 * sr + 32 * ((2 * ds + (fq >> 1)) ^ swzg(sr)) + 16 * (fq & 1)); G = __builtin_amdgcn_mfma_f32_16x16x32_bf16(a, qf[ds], G, 0, 0, 0); }
;                 const f32x4 as = *(const LAS f32x4*)(sA + c * 128 + 16 * sb + 4 * fq);
;                 float sw[4];
; #pragma unroll
;                 for (int r = 0; r < 4; ++r) { const int s = 16 * sb + 4 * fq + r; float wg = __builtin_amdgcn_exp2f((as[r] - Mt) * 1.4426950408889634f) * 0.125f; if (s > t) wg = 0.f; sw[r] = G[r] * wg; den += sw[r]; }
;                 sfr[sb >> 1][(sb & 1) * 2] = cvt_pk_bf16(sw[0], sw[1]); sfr[sb >> 1][(sb & 1) * 2 + 1] = cvt_pk_bf16(sw[2], sw[3]);
;             }
;         }
.LBB0_382:
	ds_read_b128 v[74:77], v189
	ds_read_b128 v[70:73], v189 offset:64
	ds_read_b128 v[54:57], v212 offset:18432
	ds_read_b128 v[58:61], v213 offset:18432
	v_add_u32_e32 v68, 0, v106
	v_add_u32_e32 v62, 0x15000, v68
	s_andn2_b64 vcc, exec, s[26:27]
	s_waitcnt lgkmcnt(1)
	v_mfma_f32_16x16x32_bf16 v[54:57], v[54:57], v[74:77], 0
	s_waitcnt lgkmcnt(0)
	v_mfma_f32_16x16x32_bf16 v[54:57], v[58:61], v[70:73], v[54:57]
	ds_read_b128 v[58:61], v62
	s_waitcnt lgkmcnt(0)
	v_sub_f32_e32 v58, v58, v78
	v_mul_f32_e32 v58, 0x3fb8aa3b, v58
	v_exp_f32_e32 v58, v58
	s_nop 0
	v_mul_f32_e32 v58, 0x3e000000, v58
	v_cndmask_b32_e64 v58, v58, 0, s[6:7]
	v_mul_f32_e32 v62, v54, v58
	v_fma_f32 v58, v54, v58, 0
	v_sub_f32_e32 v54, v59, v78
	v_mul_f32_e32 v54, 0x3fb8aa3b, v54
	v_exp_f32_e32 v54, v54
	s_nop 0
	v_mul_f32_e32 v54, 0x3e000000, v54
	v_cndmask_b32_e64 v54, 0, v54, s[8:9]
	v_mul_f32_e32 v59, v55, v54
	v_fmac_f32_e32 v58, v55, v54
	v_sub_f32_e32 v54, v60, v78
	v_sub_f32_e32 v55, v61, v78
	v_mul_f32_e32 v54, 0x3fb8aa3b, v54
	v_mul_f32_e32 v55, 0x3fb8aa3b, v55
	v_exp_f32_e32 v54, v54
	v_exp_f32_e32 v55, v55
	v_cvt_pk_bf16_f32 v62, v62, v59
	v_mov_b32_e32 v59, 0
	v_pk_mul_f32 v[54:55], v[54:55], s[22:23] op_sel_hi:[1,0]
	s_nop 0
	v_cndmask_b32_e64 v55, v55, 0, s[10:11]
	v_cndmask_b32_e64 v54, v54, 0, s[12:13]
	v_pk_mul_f32 v[54:55], v[56:57], v[54:55]
	s_nop 0
	v_add_f32_e32 v56, v54, v58
	v_add_f32_e32 v79, v55, v56
	v_cvt_pk_bf16_f32 v63, v54, v55
	s_cbranch_vccnz .LBB0_390
	ds_read_b128 v[54:57], v212 offset:20480
	ds_read_b128 v[64:67], v213 offset:20480
	v_add_u32_e32 v58, 0x15040, v68
	v_readlane_b32 s72, v254, 10
	v_readlane_b32 s73, v254, 11
	s_waitcnt lgkmcnt(1)
	v_mfma_f32_16x16x32_bf16 v[54:57], v[54:57], v[74:77], 0
	s_waitcnt lgkmcnt(0)
	v_mfma_f32_16x16x32_bf16 v[54:57], v[64:67], v[70:73], v[54:57]
	ds_read_b128 v[64:67], v58
	s_waitcnt lgkmcnt(0)
	v_sub_f32_e32 v58, v64, v78
	v_mul_f32_e32 v58, 0x3fb8aa3b, v58
	v_exp_f32_e32 v60, v58
	v_sub_f32_e32 v58, v65, v78
	v_mul_f32_e32 v58, 0x3fb8aa3b, v58
	v_exp_f32_e32 v61, v58
	s_nop 0
	v_pk_mul_f32 v[60:61], v[60:61], s[22:23] op_sel_hi:[1,0]
	s_nop 0
	v_cndmask_b32_e64 v61, v61, 0, s[72:73]
	v_readlane_b32 s72, v254, 12
	v_readlane_b32 s73, v254, 13
	s_nop 1
	v_cndmask_b32_e64 v60, v60, 0, s[72:73]
	v_pk_mul_f32 v[54:55], v[54:55], v[60:61]
	v_sub_f32_e32 v60, v66, v78
	v_sub_f32_e32 v61, v67, v78
	v_mul_f32_e32 v60, 0x3fb8aa3b, v60
	v_mul_f32_e32 v61, 0x3fb8aa3b, v61
	v_exp_f32_e32 v60, v60
	v_exp_f32_e32 v61, v61
	v_readlane_b32 s72, v254, 14
	v_readlane_b32 s73, v254, 15
	v_add_f32_e32 v58, v79, v54
	v_pk_mul_f32 v[60:61], v[60:61], s[22:23] op_sel_hi:[1,0]
	v_add_f32_e32 v58, v55, v58
	v_cndmask_b32_e64 v61, v61, 0, s[72:73]
	v_readlane_b32 s72, v254, 16
	v_readlane_b32 s73, v254, 17
	v_cvt_pk_bf16_f32 v64, v54, v55
	s_nop 1
	v_cndmask_b32_e64 v60, v60, 0, s[72:73]
	v_pk_mul_f32 v[56:57], v[56:57], v[60:61]
	s_nop 0
	v_add_f32_e32 v58, v56, v58
	v_add_f32_e32 v79, v57, v58
	v_cvt_pk_bf16_f32 v65, v56, v57
	v_cndmask_b32_e64 v54, 0, 1, s[14:15]
	v_cmp_ne_u32_e64 s[74:75], 1, v54
	s_andn2_b64 vcc, exec, s[14:15]
	s_cbranch_vccz .LBB0_391

; #define LAS __attribute__((address_space(3)))
; __device__ __forceinline__ void p2_mlstm_chain(Frame& F, const Args& A, int ch) {
;     ...
;         den += __shfl_xor(den, 16); den += __shfl_xor(den, 32);
;         const float winter = __builtin_amdgcn_exp2f((mc - Mt) * 1.4426950408889634f);
;         { float nq = 0.f;
; #pragma unroll
;           for (int ds = 0; ds < 2; ++ds) { const u32x4 qw = __builtin_bit_cast(u32x4, qf[ds]); const f32x4 n0 = *(const LAS f32x4*)(ns + ds * 32 + fq * 8), n1 = *(const LAS f32x4*)(ns + ds * 32 + fq * 8 + 4);
;               nq += (bflo(qw.x) * n0[0] + bfhi(qw.x) * n0[1]) + (bflo(qw.y) * n0[2] + bfhi(qw.y) * n0[3]) + (bflo(qw.z) * n1[0] + bfhi(qw.z) * n1[1]) + (bflo(qw.w) * n1[2] + bfhi(qw.w) * n1[3]); }
;           nq += __shfl_xor(nq, 16); nq += __shfl_xor(nq, 32);
;           den += winter * nq * 0.125f; }
;         f32x4 acc[8];
; #pragma unroll
;         for (int vb = 0; vb < 8; ++vb) acc[vb] = (f32x4){0.f, 0.f, 0.f, 0.f};
;         { bf16x8 qw[2]; qw[0] = scale_frag(qf[0], winter * 0.125f); qw[1] = scale_frag(qf[1], winter * 0.125f);
; #pragma unroll
;           for (int vb = 0; vb < 8; ++vb)
; #pragma unroll
;               for (int ds = 0; ds < 2; ++ds) { const bf16x8 a = tr_frag_V(L + ML_CT, 32 * ds + 8 * fq, 32 * ds + 8 * fq + 4, vb, tl); acc[vb] = __builtin_amdgcn_mfma_f32_16x16x32_bf16(a, qw[ds], acc[vb], 0, 0, 0); } }
.LBB0_397:
	ds_bpermute_b32 v80, v154, v79
	v_sub_f32_e32 v78, v107, v78
	v_mul_f32_e32 v86, 0x3fb8aa3b, v78
	v_add_u32_e32 v78, 0, v146
	v_add_u32_e32 v87, 0x14800, v78
	s_waitcnt lgkmcnt(0)
	v_add_f32_e32 v143, v79, v80
	ds_read_b128 v[78:81], v87
	ds_read_b128 v[82:85], v87 offset:16
	v_and_b32_e32 v89, 0xffff0000, v74
	v_and_b32_e32 v92, 0xffff0000, v75
	v_lshlrev_b32_e32 v88, 16, v74
	s_waitcnt lgkmcnt(1)
	v_mul_f32_e32 v74, v79, v89
	v_lshlrev_b32_e32 v91, 16, v75
	v_mul_f32_e32 v75, v81, v92
	v_fmac_f32_e32 v74, v78, v88
	v_fmac_f32_e32 v75, v80, v91
	v_and_b32_e32 v94, 0xffff0000, v76
	v_add_f32_e32 v74, v74, v75
	v_lshlrev_b32_e32 v93, 16, v76
	s_waitcnt lgkmcnt(0)
	v_mul_f32_e32 v75, v83, v94
	v_fmac_f32_e32 v75, v82, v93
	v_and_b32_e32 v83, 0xffff0000, v77
	v_add_f32_e32 v74, v75, v74
	v_lshlrev_b32_e32 v82, 16, v77
	v_mul_f32_e32 v75, v85, v83
	v_fmac_f32_e32 v75, v84, v82
	v_add_f32_e32 v74, v75, v74
	v_add_f32_e32 v84, 0, v74
	ds_read_b128 v[74:77], v87 offset:128
	ds_read_b128 v[78:81], v87 offset:144
	v_lshlrev_b32_e32 v85, 16, v70
	v_and_b32_e32 v70, 0xffff0000, v70
	v_exp_f32_e32 v145, v86
	s_waitcnt lgkmcnt(1)
	v_mul_f32_e32 v75, v75, v70
	v_fmac_f32_e32 v75, v74, v85
	v_lshlrev_b32_e32 v74, 16, v71
	v_and_b32_e32 v71, 0xffff0000, v71
	v_mul_f32_e32 v77, v77, v71
	v_fmac_f32_e32 v77, v76, v74
	v_lshlrev_b32_e32 v76, 16, v72
	v_and_b32_e32 v72, 0xffff0000, v72
	v_add_f32_e32 v75, v75, v77
	s_waitcnt lgkmcnt(0)
	v_mul_f32_e32 v77, v79, v72
	v_fmac_f32_e32 v77, v78, v76
	v_add_f32_e32 v75, v77, v75
	v_lshlrev_b32_e32 v77, 16, v73
	v_and_b32_e32 v73, 0xffff0000, v73
	v_mul_f32_e32 v78, v81, v73
	v_fmac_f32_e32 v78, v80, v77
	v_add_f32_e32 v75, v78, v75
	v_add_f32_e32 v75, v84, v75
	ds_bpermute_b32 v78, v154, v75
	v_add_u32_e32 v98, v157, v156
	v_add_u32_e32 v99, v149, v156
	v_add_u32_e32 v100, v157, v158
	v_add_u32_e32 v101, v149, v158
	s_waitcnt lgkmcnt(0)
	v_add_f32_e32 v222, v75, v78
	v_mul_f32_e32 v75, 0x3e000000, v145
	v_mul_f32_e32 v78, v75, v88
	v_mul_f32_e32 v79, v75, v89
	v_cvt_pk_bf16_f32 v90, v78, v79
	v_mul_f32_e32 v78, v75, v91
	v_mul_f32_e32 v79, v75, v92
	v_cvt_pk_bf16_f32 v91, v78, v79
	v_mul_f32_e32 v78, v75, v93
	v_mul_f32_e32 v79, v75, v94
	v_cvt_pk_bf16_f32 v92, v78, v79
	v_mul_f32_e32 v78, v75, v82
	v_mul_f32_e32 v70, v75, v70
	v_mul_f32_e32 v79, v75, v83
	v_cvt_pk_bf16_f32 v93, v78, v79
	v_mul_f32_e32 v78, v75, v85
	v_cvt_pk_bf16_f32 v86, v78, v70
	v_mul_f32_e32 v70, v75, v74
	v_mul_f32_e32 v71, v75, v71
	v_cvt_pk_bf16_f32 v87, v70, v71
	v_mul_f32_e32 v70, v75, v76
	v_mul_f32_e32 v71, v75, v72
	v_cvt_pk_bf16_f32 v88, v70, v71
	v_mul_f32_e32 v70, v75, v77
	v_mul_f32_e32 v71, v75, v73
	v_cvt_pk_bf16_f32 v89, v70, v71
	ds_read_b64_tr_b16 v[70:71], v98
	ds_read_b64_tr_b16 v[72:73], v99 offset:1024
	ds_read_b64_tr_b16 v[74:75], v100
	ds_read_b64_tr_b16 v[76:77], v101 offset:1024
	s_waitcnt lgkmcnt(2)
	v_mfma_f32_16x16x32_bf16 v[70:73], v[70:73], v[90:93], 0
	v_add_u32_e32 v102, v159, v156
	v_add_u32_e32 v103, v150, v156
	v_add_u32_e32 v104, v159, v158
	s_waitcnt lgkmcnt(0)
	v_mfma_f32_16x16x32_bf16 v[70:73], v[74:77], v[86:89], v[70:73]
	ds_read_b64_tr_b16 v[74:75], v102
	ds_read_b64_tr_b16 v[76:77], v103 offset:1024
	ds_read_b64_tr_b16 v[78:79], v104
	v_add_u32_e32 v105, v150, v158
	ds_read_b64_tr_b16 v[80:81], v105 offset:1024
	s_waitcnt lgkmcnt(2)
	v_mfma_f32_16x16x32_bf16 v[74:77], v[74:77], v[90:93], 0
	v_add_u32_e32 v224, v160, v156
	v_add_u32_e32 v225, v151, v156
	v_add_u32_e32 v226, v160, v158
	s_waitcnt lgkmcnt(0)
	v_mfma_f32_16x16x32_bf16 v[74:77], v[78:81], v[86:89], v[74:77]
	ds_read_b64_tr_b16 v[78:79], v224
	ds_read_b64_tr_b16 v[80:81], v225 offset:1024
	ds_read_b64_tr_b16 v[82:83], v226
	v_add_u32_e32 v227, v151, v158
	ds_read_b64_tr_b16 v[84:85], v227 offset:1024
	s_waitcnt lgkmcnt(2)
	v_mfma_f32_16x16x32_bf16 v[78:81], v[78:81], v[90:93], 0
	v_add_u32_e32 v228, v152, v156
	v_add_u32_e32 v229, v153, v156
	v_add_u32_e32 v230, v152, v158
	s_waitcnt lgkmcnt(0)
	v_mfma_f32_16x16x32_bf16 v[78:81], v[82:85], v[86:89], v[78:81]
	ds_read_b64_tr_b16 v[82:83], v228
	ds_read_b64_tr_b16 v[84:85], v229 offset:1024
	ds_read_b64_tr_b16 v[94:95], v230
	v_add_u32_e32 v231, v153, v158
	ds_read_b64_tr_b16 v[96:97], v231 offset:1024
	s_waitcnt lgkmcnt(2)
	v_mfma_f32_16x16x32_bf16 v[82:85], v[82:85], v[90:93], 0
	ds_bpermute_b32 v144, v155, v143
	ds_bpermute_b32 v223, v155, v222
	s_and_b64 vcc, exec, s[74:75]
	s_waitcnt lgkmcnt(2)
; __device__ __forceinline__ void p2_mlstm_chain(Frame& F, const Args& A, int ch) {
;     ...
;         { bf16x8 qw[2]; qw[0] = scale_frag(qf[0], winter * 0.125f); qw[1] = scale_frag(qf[1], winter * 0.125f);
; #pragma unroll
;           for (int vb = 0; vb < 8; ++vb)
; #pragma unroll
;               for (int ds = 0; ds < 2; ++ds) { const bf16x8 a = tr_frag_V(L + ML_CT, 32 * ds + 8 * fq, 32 * ds + 8 * fq + 4, vb, tl); acc[vb] = __builtin_amdgcn_mfma_f32_16x16x32_bf16(a, qw[ds], acc[vb], 0, 0, 0); } }
; #pragma unroll
;         for (int st = 0; st < 4; ++st) {
;             if (2 * st <= w) {
;                 const bf16x8 bfr = __builtin_bit_cast(bf16x8, (u32x4){sfr[st][0], sfr[st][1], sfr[st][2], sfr[st][3]});
; #pragma unroll
;                 for (int vb = 0; vb < 8; ++vb) { const bf16x8 a = tr_frag_V(L + ML_VS, 32 * st + 4 * fq, 32 * st + 16 + 4 * fq, vb, tl); acc[vb] = __builtin_amdgcn_mfma_f32_16x16x32_bf16(a, bfr, acc[vb], 0, 0, 0); }
;             }
;         }
	v_mfma_f32_16x16x32_bf16 v[82:85], v[94:97], v[86:89], v[82:85]
	ds_read_b64_tr_b16 v[94:95], v99
	ds_read_b64_tr_b16 v[96:97], v98 offset:1024
	ds_read_b64_tr_b16 v[98:99], v101
	ds_read_b64_tr_b16 v[100:101], v100 offset:1024
	s_waitcnt lgkmcnt(2)
	v_mfma_f32_16x16x32_bf16 v[94:97], v[94:97], v[90:93], 0
	s_waitcnt lgkmcnt(0)
	v_mfma_f32_16x16x32_bf16 v[94:97], v[98:101], v[86:89], v[94:97]
	ds_read_b64_tr_b16 v[98:99], v103
	ds_read_b64_tr_b16 v[100:101], v102 offset:1024
	ds_read_b64_tr_b16 v[102:103], v105
	ds_read_b64_tr_b16 v[104:105], v104 offset:1024
	s_waitcnt lgkmcnt(2)
	v_mfma_f32_16x16x32_bf16 v[98:101], v[98:101], v[90:93], 0
	s_waitcnt lgkmcnt(0)
	v_mfma_f32_16x16x32_bf16 v[98:101], v[102:105], v[86:89], v[98:101]
	ds_read_b64_tr_b16 v[102:103], v225
	ds_read_b64_tr_b16 v[104:105], v224 offset:1024
	ds_read_b64_tr_b16 v[224:225], v227
	ds_read_b64_tr_b16 v[226:227], v226 offset:1024
	s_waitcnt lgkmcnt(2)
	v_mfma_f32_16x16x32_bf16 v[102:105], v[102:105], v[90:93], 0
	s_waitcnt lgkmcnt(0)
	v_mfma_f32_16x16x32_bf16 v[102:105], v[224:227], v[86:89], v[102:105]
	ds_read_b64_tr_b16 v[224:225], v229
	ds_read_b64_tr_b16 v[226:227], v228 offset:1024
	s_waitcnt lgkmcnt(0)
	v_mfma_f32_16x16x32_bf16 v[90:93], v[224:227], v[90:93], 0
	ds_read_b64_tr_b16 v[224:225], v231
	ds_read_b64_tr_b16 v[226:227], v230 offset:1024
	s_waitcnt lgkmcnt(0)
	v_mfma_f32_16x16x32_bf16 v[226:229], v[224:227], v[86:89], v[90:93]
	v_add_u32_e32 v224, v161, v162
	ds_read_b64_tr_b16 v[240:241], v224 offset:34816
	ds_read_b64_tr_b16 v[242:243], v224 offset:38912
	ds_read_b64_tr_b16 v[244:245], v214 offset:34816
	ds_read_b64_tr_b16 v[246:247], v214 offset:38912
	ds_read_b64_tr_b16 v[248:249], v215 offset:34816
	ds_read_b64_tr_b16 v[250:251], v215 offset:38912
	s_waitcnt lgkmcnt(4)
	v_mfma_f32_16x16x32_bf16 v[70:73], v[240:243], v[62:65], v[70:73]
	ds_read_b64_tr_b16 v[240:241], v216 offset:34816
	ds_read_b64_tr_b16 v[242:243], v216 offset:38912
	s_waitcnt lgkmcnt(4)
	v_mfma_f32_16x16x32_bf16 v[74:77], v[244:247], v[62:65], v[74:77]
	ds_read_b64_tr_b16 v[244:245], v217 offset:34816
	ds_read_b64_tr_b16 v[246:247], v217 offset:38912
	s_waitcnt lgkmcnt(4)
	v_mfma_f32_16x16x32_bf16 v[78:81], v[248:251], v[62:65], v[78:81]
	ds_read_b64_tr_b16 v[248:249], v218 offset:34816
	ds_read_b64_tr_b16 v[250:251], v218 offset:38912
	s_waitcnt lgkmcnt(4)
	v_mfma_f32_16x16x32_bf16 v[82:85], v[240:243], v[62:65], v[82:85]
	ds_read_b64_tr_b16 v[240:241], v219 offset:34816
	ds_read_b64_tr_b16 v[242:243], v219 offset:38912
	s_waitcnt lgkmcnt(4)
	v_mfma_f32_16x16x32_bf16 v[86:89], v[244:247], v[62:65], v[94:97]
	ds_read_b64_tr_b16 v[244:245], v220 offset:34816
	ds_read_b64_tr_b16 v[246:247], v220 offset:38912
	s_waitcnt lgkmcnt(4)
	v_mfma_f32_16x16x32_bf16 v[90:93], v[248:251], v[62:65], v[98:101]
	s_waitcnt lgkmcnt(2)
	v_mfma_f32_16x16x32_bf16 v[94:97], v[240:243], v[62:65], v[102:105]
	s_waitcnt lgkmcnt(0)
	v_mfma_f32_16x16x32_bf16 v[62:65], v[244:247], v[62:65], v[226:229]
	s_cbranch_vccnz .LBB0_435
	ds_read_b64_tr_b16 v[240:241], v224 offset:43008
	ds_read_b64_tr_b16 v[242:243], v224 offset:47104
	ds_read_b64_tr_b16 v[244:245], v214 offset:43008
	ds_read_b64_tr_b16 v[246:247], v214 offset:47104
	ds_read_b64_tr_b16 v[248:249], v215 offset:43008
	ds_read_b64_tr_b16 v[250:251], v215 offset:47104
	s_waitcnt lgkmcnt(4)
	v_mfma_f32_16x16x32_bf16 v[70:73], v[240:243], v[58:61], v[70:73]
	ds_read_b64_tr_b16 v[240:241], v216 offset:43008
	ds_read_b64_tr_b16 v[242:243], v216 offset:47104
	s_waitcnt lgkmcnt(4)
	v_mfma_f32_16x16x32_bf16 v[74:77], v[244:247], v[58:61], v[74:77]
	ds_read_b64_tr_b16 v[244:245], v217 offset:43008
	ds_read_b64_tr_b16 v[246:247], v217 offset:47104
	s_waitcnt lgkmcnt(4)
	v_mfma_f32_16x16x32_bf16 v[78:81], v[248:251], v[58:61], v[78:81]
	ds_read_b64_tr_b16 v[248:249], v218 offset:43008
	ds_read_b64_tr_b16 v[250:251], v218 offset:47104
	s_waitcnt lgkmcnt(4)
	v_mfma_f32_16x16x32_bf16 v[82:85], v[240:243], v[58:61], v[82:85]
	ds_read_b64_tr_b16 v[240:241], v219 offset:43008
	ds_read_b64_tr_b16 v[242:243], v219 offset:47104
	s_waitcnt lgkmcnt(4)
	v_mfma_f32_16x16x32_bf16 v[86:89], v[244:247], v[58:61], v[86:89]
	ds_read_b64_tr_b16 v[244:245], v220 offset:43008
	ds_read_b64_tr_b16 v[246:247], v220 offset:47104
	s_waitcnt lgkmcnt(4)
	v_mfma_f32_16x16x32_bf16 v[90:93], v[248:251], v[58:61], v[90:93]
	s_waitcnt lgkmcnt(2)
	v_mfma_f32_16x16x32_bf16 v[94:97], v[240:243], v[58:61], v[94:97]
	s_waitcnt lgkmcnt(0)
	v_mfma_f32_16x16x32_bf16 v[62:65], v[244:247], v[58:61], v[62:65]
	s_and_b64 vcc, exec, s[72:73]
	s_cbranch_vccz .LBB0_436

; __device__ __forceinline__ void p2_mlstm_chain(Frame& F, const Args& A, int ch) {
;     ...
;         for (int st = 0; st < 4; ++st) {
;             if (2 * st <= w) {
;                 const bf16x8 bfr = __builtin_bit_cast(bf16x8, (u32x4){sfr[st][0], sfr[st][1], sfr[st][2], sfr[st][3]});
; #pragma unroll
;                 for (int vb = 0; vb < 8; ++vb) { const bf16x8 a = tr_frag_V(L + ML_VS, 32 * st + 4 * fq, 32 * st + 16 + 4 * fq, vb, tl); acc[vb] = __builtin_amdgcn_mfma_f32_16x16x32_bf16(a, bfr, acc[vb], 0, 0, 0); }
;             }
;         }
;         { const float inv = 1.0f / fmaxf(fabsf(den), __builtin_amdgcn_exp2f(lf * 1.4426950408889634f)); float ss = 0.f;
; #pragma unroll
;           for (int vb = 0; vb < 8; ++vb) { acc[vb] = acc[vb] * inv; ss += (acc[vb][0] * acc[vb][0] + acc[vb][1] * acc[vb][1]) + (acc[vb][2] * acc[vb][2] + acc[vb][3] * acc[vb][3]); }
;           ss += __shfl_xor(ss, 16); ss += __shfl_xor(ss, 32);
;           const float r = rsqrtf(ss * (1.0f / 128.0f) + EPS);
;           bf16* yo = ycat + (tg0 + t) * D + h * 128 + 4 * fq;
; #pragma unroll
.LBB0_400:
	ds_read_b64_tr_b16 v[240:241], v224 offset:59392
	ds_read_b64_tr_b16 v[242:243], v224 offset:63488
	ds_read_b64_tr_b16 v[244:245], v214 offset:59392
	ds_read_b64_tr_b16 v[246:247], v214 offset:63488
	ds_read_b64_tr_b16 v[248:249], v215 offset:59392
	ds_read_b64_tr_b16 v[250:251], v215 offset:63488
	s_waitcnt lgkmcnt(4)
	v_mfma_f32_16x16x32_bf16 v[70:73], v[240:243], v[66:69], v[70:73]
	ds_read_b64_tr_b16 v[240:241], v216 offset:59392
	ds_read_b64_tr_b16 v[242:243], v216 offset:63488
	s_waitcnt lgkmcnt(4)
	v_mfma_f32_16x16x32_bf16 v[74:77], v[244:247], v[66:69], v[74:77]
	ds_read_b64_tr_b16 v[244:245], v217 offset:59392
	ds_read_b64_tr_b16 v[246:247], v217 offset:63488
	s_waitcnt lgkmcnt(4)
	v_mfma_f32_16x16x32_bf16 v[78:81], v[248:251], v[66:69], v[78:81]
	ds_read_b64_tr_b16 v[248:249], v218 offset:59392
	ds_read_b64_tr_b16 v[250:251], v218 offset:63488
	s_waitcnt lgkmcnt(4)
	v_mfma_f32_16x16x32_bf16 v[82:85], v[240:243], v[66:69], v[82:85]
	ds_read_b64_tr_b16 v[240:241], v219 offset:59392
	ds_read_b64_tr_b16 v[242:243], v219 offset:63488
	s_waitcnt lgkmcnt(4)
	v_mfma_f32_16x16x32_bf16 v[86:89], v[244:247], v[66:69], v[86:89]
	ds_read_b64_tr_b16 v[244:245], v220 offset:59392
	ds_read_b64_tr_b16 v[246:247], v220 offset:63488
	s_waitcnt lgkmcnt(4)
	v_mfma_f32_16x16x32_bf16 v[90:93], v[248:251], v[66:69], v[90:93]
	s_waitcnt lgkmcnt(2)
	v_mfma_f32_16x16x32_bf16 v[94:97], v[240:243], v[66:69], v[94:97]
	s_waitcnt lgkmcnt(0)
	v_mfma_f32_16x16x32_bf16 v[62:65], v[244:247], v[66:69], v[62:65]
.LBB0_401:
	ds_read_b128 v[232:235], v252
	ds_read_b128 v[236:239], v252 offset:64
	v_add_f32_e32 v54, v222, v223
	v_mul_f32_e32 v54, v145, v54
	v_add_f32_e32 v55, v143, v144
	v_fmac_f32_e32 v55, 0x3e000000, v54
	v_mul_f32_e32 v54, 0x3fb8aa3b, v142
	v_exp_f32_e32 v54, v54
	s_nop 0
	v_max_f32_e64 v54, |v55|, v54
	v_div_scale_f32 v55, s[72:73], v54, v54, 1.0
	v_rcp_f32_e32 v56, v55
	s_mov_b32 s72, 0x800000
	v_fma_f32 v57, -v55, v56, 1.0
	v_fmac_f32_e32 v56, v57, v56
	v_div_scale_f32 v57, vcc, 1.0, v54, 1.0
	v_mul_f32_e32 v58, v57, v56
	v_fma_f32 v59, -v55, v58, v57
	v_fmac_f32_e32 v58, v59, v56
	v_fma_f32 v55, -v55, v58, v57
	v_div_fmas_f32 v55, v55, v56, v58
	v_div_fixup_f32 v54, v55, v54, 1.0
	v_pk_mul_f32 v[144:145], v[54:55], v[70:71] op_sel_hi:[0,1]
	v_pk_mul_f32 v[104:105], v[54:55], v[74:75] op_sel_hi:[0,1]
	v_pk_mul_f32 v[142:143], v[54:55], v[72:73] op_sel_hi:[0,1]
	v_pk_mul_f32 v[102:103], v[54:55], v[76:77] op_sel_hi:[0,1]
	v_mov_b32_e32 v58, v145
	v_mov_b32_e32 v59, v105
	v_mov_b32_e32 v56, v144
	v_mov_b32_e32 v57, v104
	v_pk_mul_f32 v[58:59], v[58:59], v[58:59]
	v_mov_b32_e32 v60, v143
	v_mov_b32_e32 v61, v103
	v_pk_fma_f32 v[56:57], v[56:57], v[56:57], v[58:59]
	v_mov_b32_e32 v58, v142
	v_mov_b32_e32 v59, v102
	v_pk_mul_f32 v[60:61], v[60:61], v[60:61]
	v_pk_mul_f32 v[98:99], v[54:55], v[80:81] op_sel_hi:[0,1]
	v_pk_fma_f32 v[58:59], v[58:59], v[58:59], v[60:61]
	v_pk_mul_f32 v[100:101], v[54:55], v[78:79] op_sel_hi:[0,1]
	v_pk_add_f32 v[56:57], v[56:57], v[58:59]
	v_pk_mul_f32 v[58:59], v[98:99], v[98:99]
	v_pk_add_f32 v[56:57], v[56:57], v[56:57] op_sel_hi:[0,1]
	v_pk_mul_f32 v[60:61], v[100:101], v[100:101]
	v_pk_mul_f32 v[80:81], v[54:55], v[82:83] op_sel_hi:[0,1]
	v_pk_mov_b32 v[66:67], v[60:61], v[58:59] op_sel:[1,0]
	v_mov_b32_e32 v61, v59
	v_pk_mul_f32 v[78:79], v[54:55], v[84:85] op_sel_hi:[0,1]
	v_mul_f32_e32 v56, v80, v80
	v_pk_add_f32 v[58:59], v[66:67], v[60:61]
	v_pk_fma_f32 v[60:61], v[80:81], v[80:81], v[56:57] op_sel_hi:[1,1,0]
	v_mul_f32_e32 v56, v78, v78
	v_pk_add_f32 v[58:59], v[58:59], v[58:59] op_sel_hi:[0,1]
	v_pk_fma_f32 v[66:67], v[78:79], v[78:79], v[56:57] op_sel_hi:[1,1,0]
	v_pk_mul_f32 v[74:75], v[54:55], v[88:89] op_sel_hi:[0,1]
	v_pk_mul_f32 v[76:77], v[54:55], v[86:87] op_sel_hi:[0,1]
	v_mul_f32_e32 v60, v76, v76
	v_mul_f32_e32 v66, v77, v77
	v_mul_f32_e32 v58, v74, v74
	v_mul_f32_e32 v56, v75, v75
	v_pk_add_f32 v[60:61], v[60:61], v[66:67]
	v_pk_add_f32 v[56:57], v[58:59], v[56:57]
	v_pk_mul_f32 v[70:71], v[54:55], v[92:93] op_sel_hi:[0,1]
	v_pk_mul_f32 v[72:73], v[54:55], v[90:91] op_sel_hi:[0,1]
	v_pk_add_f32 v[56:57], v[60:61], v[56:57]
	v_pk_mul_f32 v[58:59], v[70:71], v[70:71]
	v_pk_mul_f32 v[60:61], v[72:73], v[72:73]
	v_pk_add_f32 v[56:57], v[56:57], v[56:57] op_sel_hi:[0,1]
	v_pk_mov_b32 v[66:67], v[60:61], v[58:59] op_sel:[1,0]
	v_mov_b32_e32 v61, v59
	v_pk_mul_f32 v[68:69], v[54:55], v[94:95] op_sel_hi:[0,1]
	v_pk_add_f32 v[58:59], v[66:67], v[60:61]
	v_pk_mul_f32 v[66:67], v[54:55], v[96:97] op_sel_hi:[0,1]
	v_mul_f32_e32 v56, v68, v68
	v_pk_fma_f32 v[84:85], v[68:69], v[68:69], v[56:57] op_sel_hi:[1,1,0]
	v_mul_f32_e32 v56, v66, v66
	v_pk_add_f32 v[82:83], v[58:59], v[58:59] op_sel_hi:[0,1]
	v_pk_fma_f32 v[86:87], v[66:67], v[66:67], v[56:57] op_sel_hi:[1,1,0]
	v_pk_mul_f32 v[58:59], v[54:55], v[64:65] op_sel_hi:[0,1]
	v_pk_mul_f32 v[60:61], v[54:55], v[62:63] op_sel_hi:[0,1]
	v_mul_f32_e32 v84, v60, v60
	v_mul_f32_e32 v86, v61, v61
	v_mul_f32_e32 v82, v58, v58
	v_mul_f32_e32 v56, v59, v59
	v_pk_add_f32 v[54:55], v[84:85], v[86:87]
	v_pk_add_f32 v[56:57], v[82:83], v[56:57]
	s_nop 0
	v_pk_add_f32 v[54:55], v[54:55], v[56:57]
	s_nop 0
	v_add_f32_e32 v54, v54, v55
	ds_bpermute_b32 v55, v154, v54
	s_waitcnt lgkmcnt(0)
	v_add_f32_e32 v54, v54, v55
	ds_bpermute_b32 v55, v155, v54
	s_waitcnt lgkmcnt(0)
	v_add_f32_e32 v54, v54, v55
	v_fmamk_f32 v54, v54, 0x3c000000, v190
	v_cmp_gt_f32_e32 vcc, s72, v54
	v_mul_f32_e32 v55, 0x4b800000, v54
	s_nop 0
	v_cndmask_b32_e32 v54, v54, v55, vcc
	v_rsq_f32_e32 v54, v54
	s_nop 0
	v_mul_f32_e32 v55, 0x45800000, v54
	v_cndmask_b32_e32 v62, v54, v55, vcc
	v_mul_f32_e32 v63, v144, v62
	v_mul_f32_e32 v60, v60, v62
	v_mul_f32_e32 v58, v58, v62
	s_andn2_b64 vcc, exec, s[24:25]
	s_waitcnt vmcnt(8) lgkmcnt(0)
	s_cmp_lg_u32 s42, 0x960000
	s_cbranch_scc1 .Lmy_ogw
	s_waitcnt vmcnt(0)
; #define GAS __attribute__((address_space(1)))
; __device__ __forceinline__ unsigned cvt_pk_bf16(float lo, float hi) { unsigned r; asm volatile("v_cvt_pk_bf16_f32 %0, %1, %2" : "=v"(r) : "v"(lo), "v"(hi)); return r; }
; __device__ __forceinline__ float sigmoidf_fast(float x) { return __builtin_amdgcn_rcpf(1.0f + __builtin_amdgcn_exp2f(-1.4426950408889634f * x)); }
; __device__ __forceinline__ void p2_mlstm_chain(Frame& F, const Args& A, int ch) {
;     ...
;         { const float inv = 1.0f / fmaxf(fabsf(den), __builtin_amdgcn_exp2f(lf * 1.4426950408889634f)); float ss = 0.f;
; #pragma unroll
;           for (int vb = 0; vb < 8; ++vb) { acc[vb] = acc[vb] * inv; ss += (acc[vb][0] * acc[vb][0] + acc[vb][1] * acc[vb][1]) + (acc[vb][2] * acc[vb][2] + acc[vb][3] * acc[vb][3]); }
;           ss += __shfl_xor(ss, 16); ss += __shfl_xor(ss, 32);
;           const float r = rsqrtf(ss * (1.0f / 128.0f) + EPS);
;           bf16* yo = ycat + (tg0 + t) * D + h * 128 + 4 * fq;
; #pragma unroll
;           for (int vb = 0; vb < 8; ++vb) { const f32x4 gh = *(const f32x4*)(ghead + 16 * vb + 4 * fq);
;               const float y0 = acc[vb][0] * r * gh[0] * sigmoidf_fast(bflo(og[vb].x)), y1 = acc[vb][1] * r * gh[1] * sigmoidf_fast(bfhi(og[vb].x));
;               const float y2 = acc[vb][2] * r * gh[2] * sigmoidf_fast(bflo(og[vb].y)), y3 = acc[vb][3] * r * gh[3] * sigmoidf_fast(bfhi(og[vb].y));
;               *(GAS u32x2*)(yo + 16 * vb) = (u32x2){cvt_pk_bf16(y0, y1), cvt_pk_bf16(y2, y3)}; } }
.Lmy_ogw:
	v_mul_f32_e32 v54, v232, v63
	v_lshlrev_b32_e32 v63, 16, v140
	v_mul_f32_e32 v63, 0xbfb8aa3b, v63
	v_exp_f32_e32 v63, v63
	s_nop 0
	v_add_f32_e32 v63, 1.0, v63
	v_rcp_f32_e32 v63, v63
	s_nop 0
	v_mul_f32_e32 v54, v63, v54
	v_mul_f32_e32 v63, v145, v62
	v_mul_f32_e32 v55, v233, v63
	v_and_b32_e32 v63, 0xffff0000, v140
	v_mul_f32_e32 v63, 0xbfb8aa3b, v63
	v_exp_f32_e32 v63, v63
	s_nop 0
	v_add_f32_e32 v63, 1.0, v63
	v_rcp_f32_e32 v63, v63
	s_nop 0
	v_mul_f32_e32 v55, v63, v55
	v_mul_f32_e32 v63, v142, v62
	v_mul_f32_e32 v56, v234, v63
	v_lshlrev_b32_e32 v63, 16, v141
	v_mul_f32_e32 v63, 0xbfb8aa3b, v63
	v_exp_f32_e32 v63, v63
	v_cvt_pk_bf16_f32 v54, v54, v55
	s_nop 0
	v_add_f32_e32 v63, 1.0, v63
	v_rcp_f32_e32 v63, v63
	s_nop 0
	v_mul_f32_e32 v56, v63, v56
	v_mul_f32_e32 v63, v143, v62
	v_mul_f32_e32 v57, v235, v63
	ds_read_b128 v[232:235], v252 offset:128
	v_and_b32_e32 v63, 0xffff0000, v141
	v_mul_f32_e32 v63, 0xbfb8aa3b, v63
	v_exp_f32_e32 v63, v63
	s_nop 0
	v_add_f32_e32 v63, 1.0, v63
	v_rcp_f32_e32 v63, v63
	s_nop 0
	v_mul_f32_e32 v57, v63, v57
	v_cvt_pk_bf16_f32 v55, v56, v57
	global_store_dwordx2 v[110:111], v[54:55], off offset:-128
	v_mul_f32_e32 v63, v104, v62
	s_waitcnt lgkmcnt(1)
	v_mul_f32_e32 v54, v236, v63
	v_lshlrev_b32_e32 v63, 16, v138
	v_mul_f32_e32 v63, 0xbfb8aa3b, v63
	v_exp_f32_e32 v63, v63
	s_nop 0
	v_add_f32_e32 v63, 1.0, v63
	v_rcp_f32_e32 v63, v63
	s_nop 0
	v_mul_f32_e32 v54, v63, v54
	v_mul_f32_e32 v63, v105, v62
	v_mul_f32_e32 v55, v237, v63
	v_and_b32_e32 v63, 0xffff0000, v138
	v_mul_f32_e32 v63, 0xbfb8aa3b, v63
	v_exp_f32_e32 v63, v63
	s_nop 0
	v_add_f32_e32 v63, 1.0, v63
	v_rcp_f32_e32 v63, v63
	s_nop 0
	v_mul_f32_e32 v55, v63, v55
	v_mul_f32_e32 v63, v102, v62
	v_mul_f32_e32 v56, v238, v63
	v_lshlrev_b32_e32 v63, 16, v139
	v_mul_f32_e32 v63, 0xbfb8aa3b, v63
	v_exp_f32_e32 v63, v63
	v_cvt_pk_bf16_f32 v54, v54, v55
	s_nop 0
	v_add_f32_e32 v63, 1.0, v63
	v_rcp_f32_e32 v63, v63
	s_nop 0
	v_mul_f32_e32 v56, v63, v56
	v_mul_f32_e32 v63, v103, v62
	v_mul_f32_e32 v57, v239, v63
	ds_read_b128 v[236:239], v252 offset:192
	v_and_b32_e32 v63, 0xffff0000, v139
	v_mul_f32_e32 v63, 0xbfb8aa3b, v63
	v_exp_f32_e32 v63, v63
	s_nop 0
	v_add_f32_e32 v63, 1.0, v63
	v_rcp_f32_e32 v63, v63
	s_nop 0
	v_mul_f32_e32 v57, v63, v57
	v_cvt_pk_bf16_f32 v55, v56, v57
	global_store_dwordx2 v[110:111], v[54:55], off offset:-96
	v_mul_f32_e32 v63, v100, v62
	s_waitcnt lgkmcnt(1)
	v_mul_f32_e32 v54, v232, v63
	v_lshlrev_b32_e32 v63, 16, v136
	v_mul_f32_e32 v63, 0xbfb8aa3b, v63
	v_exp_f32_e32 v63, v63
	s_nop 0
	v_add_f32_e32 v63, 1.0, v63
	v_rcp_f32_e32 v63, v63
	s_nop 0
	v_mul_f32_e32 v54, v63, v54
	v_mul_f32_e32 v63, v101, v62
	v_mul_f32_e32 v55, v233, v63
	v_and_b32_e32 v63, 0xffff0000, v136
	v_mul_f32_e32 v63, 0xbfb8aa3b, v63
	v_exp_f32_e32 v63, v63
	s_nop 0
	v_add_f32_e32 v63, 1.0, v63
	v_rcp_f32_e32 v63, v63
	s_nop 0
	v_mul_f32_e32 v55, v63, v55
	v_mul_f32_e32 v63, v98, v62
	v_mul_f32_e32 v56, v234, v63
	v_lshlrev_b32_e32 v63, 16, v137
	v_mul_f32_e32 v63, 0xbfb8aa3b, v63
	v_exp_f32_e32 v63, v63
	v_cvt_pk_bf16_f32 v54, v54, v55
	s_nop 0
	v_add_f32_e32 v63, 1.0, v63
	v_rcp_f32_e32 v63, v63
	s_nop 0
	v_mul_f32_e32 v56, v63, v56
	v_mul_f32_e32 v63, v99, v62
	v_mul_f32_e32 v57, v235, v63
	ds_read_b128 v[232:235], v252 offset:256
	v_and_b32_e32 v63, 0xffff0000, v137
	v_mul_f32_e32 v63, 0xbfb8aa3b, v63
	v_exp_f32_e32 v63, v63
	s_nop 0
	v_add_f32_e32 v63, 1.0, v63
	v_rcp_f32_e32 v63, v63
	s_nop 0
	v_mul_f32_e32 v57, v63, v57
	v_cvt_pk_bf16_f32 v55, v56, v57
	global_store_dwordx2 v[110:111], v[54:55], off offset:-64
	v_mul_f32_e32 v63, v80, v62
	s_waitcnt lgkmcnt(1)
	v_mul_f32_e32 v54, v236, v63
	v_lshlrev_b32_e32 v63, 16, v134
	v_mul_f32_e32 v63, 0xbfb8aa3b, v63
	v_exp_f32_e32 v63, v63
	s_nop 0
	v_add_f32_e32 v63, 1.0, v63
	v_rcp_f32_e32 v63, v63
	s_nop 0
	v_mul_f32_e32 v54, v63, v54
	v_mul_f32_e32 v63, v81, v62
	v_mul_f32_e32 v55, v237, v63
	v_and_b32_e32 v63, 0xffff0000, v134
	v_mul_f32_e32 v63, 0xbfb8aa3b, v63
	v_exp_f32_e32 v63, v63
	s_nop 0
	v_add_f32_e32 v63, 1.0, v63
	v_rcp_f32_e32 v63, v63
	s_nop 0
	v_mul_f32_e32 v55, v63, v55
	v_mul_f32_e32 v63, v78, v62
	v_mul_f32_e32 v56, v238, v63
	v_lshlrev_b32_e32 v63, 16, v135
	v_mul_f32_e32 v63, 0xbfb8aa3b, v63
	v_exp_f32_e32 v63, v63
	v_cvt_pk_bf16_f32 v54, v54, v55
	s_nop 0
	v_add_f32_e32 v63, 1.0, v63
	v_rcp_f32_e32 v63, v63
	s_nop 0
	v_mul_f32_e32 v56, v63, v56
	v_mul_f32_e32 v63, v79, v62
	v_mul_f32_e32 v57, v239, v63
	ds_read_b128 v[236:239], v252 offset:320
	v_and_b32_e32 v63, 0xffff0000, v135
	v_mul_f32_e32 v63, 0xbfb8aa3b, v63
	v_exp_f32_e32 v63, v63
	s_nop 0
	v_add_f32_e32 v63, 1.0, v63
	v_rcp_f32_e32 v63, v63
	s_nop 0
	v_mul_f32_e32 v57, v63, v57
	v_cvt_pk_bf16_f32 v55, v56, v57
	global_store_dwordx2 v[110:111], v[54:55], off offset:-32
	v_mul_f32_e32 v63, v76, v62
	s_waitcnt lgkmcnt(1)
	v_mul_f32_e32 v54, v232, v63
	v_lshlrev_b32_e32 v63, 16, v132
	v_mul_f32_e32 v63, 0xbfb8aa3b, v63
	v_exp_f32_e32 v63, v63
	s_nop 0
	v_add_f32_e32 v63, 1.0, v63
	v_rcp_f32_e32 v63, v63
	s_nop 0
	v_mul_f32_e32 v54, v63, v54
	v_mul_f32_e32 v63, v77, v62
	v_mul_f32_e32 v55, v233, v63
	v_and_b32_e32 v63, 0xffff0000, v132
	v_mul_f32_e32 v63, 0xbfb8aa3b, v63
	v_exp_f32_e32 v63, v63
	s_nop 0
	v_add_f32_e32 v63, 1.0, v63
	v_rcp_f32_e32 v63, v63
	s_nop 0
	v_mul_f32_e32 v55, v63, v55
	v_mul_f32_e32 v63, v74, v62
	v_mul_f32_e32 v56, v234, v63
	v_lshlrev_b32_e32 v63, 16, v133
	v_mul_f32_e32 v63, 0xbfb8aa3b, v63
	v_exp_f32_e32 v63, v63
	v_cvt_pk_bf16_f32 v54, v54, v55
	s_nop 0
	v_add_f32_e32 v63, 1.0, v63
	v_rcp_f32_e32 v63, v63
	s_nop 0
	v_mul_f32_e32 v56, v63, v56
	v_mul_f32_e32 v63, v75, v62
	v_mul_f32_e32 v57, v235, v63
	ds_read_b128 v[232:235], v252 offset:384
	v_and_b32_e32 v63, 0xffff0000, v133
	v_mul_f32_e32 v63, 0xbfb8aa3b, v63
	v_exp_f32_e32 v63, v63
	s_nop 0
	v_add_f32_e32 v63, 1.0, v63
	v_rcp_f32_e32 v63, v63
	s_nop 0
	v_mul_f32_e32 v57, v63, v57
	v_cvt_pk_bf16_f32 v55, v56, v57
	global_store_dwordx2 v[110:111], v[54:55], off
	v_mul_f32_e32 v63, v72, v62
	s_waitcnt lgkmcnt(1)
; #define GAS __attribute__((address_space(1)))
; #define LAS __attribute__((address_space(3)))
; __device__ __forceinline__ unsigned cvt_pk_bf16(float lo, float hi) { unsigned r; asm volatile("v_cvt_pk_bf16_f32 %0, %1, %2" : "=v"(r) : "v"(lo), "v"(hi)); return r; }
; __device__ __forceinline__ float sigmoidf_fast(float x) { return __builtin_amdgcn_rcpf(1.0f + __builtin_amdgcn_exp2f(-1.4426950408889634f * x)); }
; __device__ __forceinline__ void p2_mlstm_chain(Frame& F, const Args& A, int ch) {
;     ...
;         u32x2 og[8];
; #pragma unroll
;         for (int vb = 0; vb < 8; ++vb) og[vb] = *(const GAS u32x2*)(proj + (tg0 + t) * NP + 1024 + h * 128 + 16 * vb + 4 * fq);
;     ...
;           for (int vb = 0; vb < 8; ++vb) { const f32x4 gh = *(const f32x4*)(ghead + 16 * vb + 4 * fq);
;               const float y0 = acc[vb][0] * r * gh[0] * sigmoidf_fast(bflo(og[vb].x)), y1 = acc[vb][1] * r * gh[1] * sigmoidf_fast(bfhi(og[vb].x));
;               const float y2 = acc[vb][2] * r * gh[2] * sigmoidf_fast(bflo(og[vb].y)), y3 = acc[vb][3] * r * gh[3] * sigmoidf_fast(bfhi(og[vb].y));
;               *(GAS u32x2*)(yo + 16 * vb) = (u32x2){cvt_pk_bf16(y0, y1), cvt_pk_bf16(y2, y3)}; } }
;         { const float decay = __builtin_amdgcn_exp2f((mc - Mn) * 1.4426950408889634f);
; #pragma unroll
;           for (int db = 0; db < 4; ++db) Cst[db] = Cst[db] * decay;
;           Nst = Nst * decay;
; #pragma unroll
;           for (int st = 0; st < 4; ++st) { const f32x4 k0 = *(const LAS f32x4*)(sWK + 32 * st + 8 * fq), k1 = *(const LAS f32x4*)(sWK + 32 * st + 8 * fq + 4);
;               const bf16x8 a = scale_frag8(tr_frag_V(L + ML_VS, 32 * st + 8 * fq, 32 * st + 8 * fq + 4, w, tl), k0, k1);
;               const u32x4 wkp = (u32x4){cvt_pk_bf16(k0[0], k0[1]), cvt_pk_bf16(k0[2], k0[3]), cvt_pk_bf16(k1[0], k1[1]), cvt_pk_bf16(k1[2], k1[3])};
;               const bf16x8 an = __builtin_bit_cast(bf16x8, tl == 0 ? wkp : (u32x4){0u, 0u, 0u, 0u});
; #pragma unroll
;               for (int db = 0; db < 4; ++db) { const bf16x8 bb = tr_frag_K(L + ML_KS, 32 * st + 8 * fq, 32 * st + 8 * fq + 4, db, tl); Cst[db] = __builtin_amdgcn_mfma_f32_16x16x32_bf16(a, bb, Cst[db], 0, 0, 0);
;                   if (db == w) Nst = __builtin_amdgcn_mfma_f32_16x16x32_bf16(an, bb, Nst, 0, 0, 0); } } }
	v_mul_f32_e32 v54, v63, v236
	v_lshlrev_b32_e32 v63, 16, v130
	v_mul_f32_e32 v63, 0xbfb8aa3b, v63
	v_exp_f32_e32 v63, v63
	s_nop 0
	v_add_f32_e32 v63, 1.0, v63
	v_rcp_f32_e32 v63, v63
	s_nop 0
	v_mul_f32_e32 v54, v63, v54
	v_mul_f32_e32 v63, v73, v62
	v_mul_f32_e32 v55, v63, v237
	v_and_b32_e32 v63, 0xffff0000, v130
	v_mul_f32_e32 v63, 0xbfb8aa3b, v63
	v_exp_f32_e32 v63, v63
	s_nop 0
	v_add_f32_e32 v63, 1.0, v63
	v_rcp_f32_e32 v63, v63
	s_nop 0
	v_mul_f32_e32 v55, v63, v55
	v_mul_f32_e32 v63, v70, v62
	v_mul_f32_e32 v56, v63, v238
	v_lshlrev_b32_e32 v63, 16, v131
	v_mul_f32_e32 v63, 0xbfb8aa3b, v63
	v_exp_f32_e32 v63, v63
	v_cvt_pk_bf16_f32 v54, v54, v55
	s_nop 0
	v_add_f32_e32 v63, 1.0, v63
	v_rcp_f32_e32 v63, v63
	s_nop 0
	v_mul_f32_e32 v56, v63, v56
	v_mul_f32_e32 v63, v71, v62
	v_mul_f32_e32 v57, v63, v239
	ds_read_b128 v[236:239], v252 offset:448
	v_and_b32_e32 v63, 0xffff0000, v131
	v_mul_f32_e32 v63, 0xbfb8aa3b, v63
	v_exp_f32_e32 v63, v63
	s_nop 0
	v_add_f32_e32 v63, 1.0, v63
	v_rcp_f32_e32 v63, v63
	s_nop 0
	v_mul_f32_e32 v57, v63, v57
	v_cvt_pk_bf16_f32 v55, v56, v57
	global_store_dwordx2 v[110:111], v[54:55], off offset:32
	v_mul_f32_e32 v63, v68, v62
	s_waitcnt lgkmcnt(1)
	v_mul_f32_e32 v54, v63, v232
	v_lshlrev_b32_e32 v63, 16, v128
	v_mul_f32_e32 v63, 0xbfb8aa3b, v63
	v_exp_f32_e32 v63, v63
	s_nop 0
	v_add_f32_e32 v63, 1.0, v63
	v_rcp_f32_e32 v63, v63
	s_nop 0
	v_mul_f32_e32 v54, v63, v54
	v_mul_f32_e32 v63, v69, v62
	v_mul_f32_e32 v55, v63, v233
	v_and_b32_e32 v63, 0xffff0000, v128
	v_mul_f32_e32 v63, 0xbfb8aa3b, v63
	v_exp_f32_e32 v63, v63
	s_nop 0
	v_add_f32_e32 v63, 1.0, v63
	v_rcp_f32_e32 v63, v63
	s_nop 0
	v_mul_f32_e32 v55, v63, v55
	v_mul_f32_e32 v63, v66, v62
	v_mul_f32_e32 v56, v63, v234
	v_lshlrev_b32_e32 v63, 16, v129
	v_mul_f32_e32 v63, 0xbfb8aa3b, v63
	v_exp_f32_e32 v63, v63
	v_cvt_pk_bf16_f32 v54, v54, v55
	s_nop 0
	v_add_f32_e32 v63, 1.0, v63
	v_rcp_f32_e32 v63, v63
	s_nop 0
	v_mul_f32_e32 v56, v63, v56
	v_mul_f32_e32 v63, v67, v62
	v_mul_f32_e32 v57, v63, v235
	v_and_b32_e32 v63, 0xffff0000, v129
	v_mul_f32_e32 v63, 0xbfb8aa3b, v63
	v_exp_f32_e32 v63, v63
	s_nop 0
	v_add_f32_e32 v63, 1.0, v63
	v_rcp_f32_e32 v63, v63
	s_nop 0
	v_mul_f32_e32 v57, v63, v57
	v_cvt_pk_bf16_f32 v55, v56, v57
	global_store_dwordx2 v[110:111], v[54:55], off offset:64
	s_waitcnt lgkmcnt(0)
	v_mul_f32_e32 v54, v60, v236
	v_lshlrev_b32_e32 v60, 16, v126
	v_mul_f32_e32 v60, 0xbfb8aa3b, v60
	v_mul_f32_e32 v56, v58, v238
	v_lshlrev_b32_e32 v58, 16, v127
	v_exp_f32_e32 v60, v60
	v_mul_f32_e32 v58, 0xbfb8aa3b, v58
	v_exp_f32_e32 v58, v58
	v_add_f32_e32 v60, 1.0, v60
	v_rcp_f32_e32 v60, v60
	v_add_f32_e32 v58, 1.0, v58
	v_rcp_f32_e32 v58, v58
	v_mul_f32_e32 v54, v60, v54
	v_mul_f32_e32 v60, v61, v62
	v_mul_f32_e32 v55, v60, v237
	v_and_b32_e32 v60, 0xffff0000, v126
	v_mul_f32_e32 v56, v58, v56
	v_mul_f32_e32 v58, v59, v62
	v_mul_f32_e32 v60, 0xbfb8aa3b, v60
	v_mul_f32_e32 v57, v58, v239
	v_and_b32_e32 v58, 0xffff0000, v127
	v_exp_f32_e32 v60, v60
	v_mul_f32_e32 v58, 0xbfb8aa3b, v58
	v_exp_f32_e32 v58, v58
	v_add_f32_e32 v60, 1.0, v60
	v_rcp_f32_e32 v60, v60
	v_add_f32_e32 v58, 1.0, v58
	v_rcp_f32_e32 v58, v58
	v_mul_f32_e32 v55, v60, v55
	v_cvt_pk_bf16_f32 v54, v54, v55
	v_mul_f32_e32 v57, v58, v57
	v_cvt_pk_bf16_f32 v55, v56, v57
	global_store_dwordx2 v[110:111], v[54:55], off offset:96
	s_cmp_eq_u32 s42, 0x960000
	s_cbranch_scc1 .Lmy_noog
	s_mov_b64 s[98:99], 0xa0000
	v_lshl_add_u64 v[240:241], v[120:121], 0, s[42:43]
	v_lshl_add_u64 v[240:241], v[240:241], 0, s[98:99]
	global_load_dwordx2 v[140:141], v[240:241], off offset:-128
	global_load_dwordx2 v[138:139], v[240:241], off offset:-96
	global_load_dwordx2 v[136:137], v[240:241], off offset:-64
	global_load_dwordx2 v[134:135], v[240:241], off offset:-32
	global_load_dwordx2 v[132:133], v[240:241], off
	global_load_dwordx2 v[130:131], v[240:241], off offset:32
	global_load_dwordx2 v[128:129], v[240:241], off offset:64
	global_load_dwordx2 v[126:127], v[240:241], off offset:96
.Lmy_noog:
	v_sub_f32_e32 v54, v107, v221
	v_mul_f32_e32 v54, 0x3fb8aa3b, v54
	v_exp_f32_e32 v66, v54
	s_nop 0
	v_pk_mul_f32 v[60:61], v[52:53], v[66:67] op_sel_hi:[1,0]
	v_pk_mul_f32 v[58:59], v[50:51], v[66:67] op_sel_hi:[1,0]
	ds_read_b128 v[50:53], v147
	ds_read_b128 v[62:65], v147 offset:16
	ds_read_b64_tr_b16 v[54:55], v191 offset:34816
	ds_read_b64_tr_b16 v[56:57], v192 offset:34816
	v_pk_mul_f32 v[36:37], v[36:37], v[66:67] op_sel_hi:[1,0]
	v_pk_mul_f32 v[34:35], v[34:35], v[66:67] op_sel_hi:[1,0]
	s_waitcnt lgkmcnt(1)
	v_lshlrev_b32_e32 v67, 16, v54
	v_and_b32_e32 v54, 0xffff0000, v54
	v_mul_f32_e32 v67, v50, v67
	v_mul_f32_e32 v54, v51, v54
	v_cvt_pk_bf16_f32 v54, v67, v54
	v_lshlrev_b32_e32 v67, 16, v55
	v_and_b32_e32 v55, 0xffff0000, v55
	v_mul_f32_e32 v67, v52, v67
	v_mul_f32_e32 v55, v53, v55
	v_cvt_pk_bf16_f32 v55, v67, v55
	s_waitcnt lgkmcnt(0)
	v_lshlrev_b32_e32 v67, 16, v56
	v_and_b32_e32 v56, 0xffff0000, v56
	v_mul_f32_e32 v67, v62, v67
	v_mul_f32_e32 v56, v63, v56
	v_cvt_pk_bf16_f32 v56, v67, v56
	v_lshlrev_b32_e32 v67, 16, v57
	v_and_b32_e32 v57, 0xffff0000, v57
	v_mul_f32_e32 v57, v65, v57
	v_mul_f32_e32 v67, v64, v67
	v_cvt_pk_bf16_f32 v57, v67, v57
	v_cvt_pk_bf16_f32 v50, v50, v51
	v_cvt_pk_bf16_f32 v51, v52, v53
	v_cvt_pk_bf16_f32 v52, v62, v63
	v_cvt_pk_bf16_f32 v53, v64, v65
	v_add_u32_e32 v62, v163, v165
	v_add_u32_e32 v64, v164, v166
	ds_read_b64_tr_b16 v[62:63], v62 offset:18432
	ds_read_b64_tr_b16 v[64:65], v64 offset:18432
	s_waitcnt lgkmcnt(0)
	v_mfma_f32_16x16x32_bf16 v[58:61], v[54:57], v[62:65], v[58:61]
	v_cndmask_b32_e64 v67, 0, 1, s[24:25]
	v_cndmask_b32_e64 v50, 0, v50, s[4:5]
	v_cndmask_b32_e64 v51, 0, v51, s[4:5]
	v_cndmask_b32_e64 v52, 0, v52, s[4:5]
	v_cndmask_b32_e64 v53, 0, v53, s[4:5]
	v_cmp_ne_u32_e64 s[72:73], 1, v67
	s_cbranch_vccnz .LBB0_403
	v_mfma_f32_16x16x32_bf16 v[34:37], v[50:53], v[62:65], v[34:37]

; __device__ __forceinline__ void p2_mlstm_chain(Frame& F, const Args& A, int ch) {
;     ...
;         for (int st = 0; st < 4; ++st) {
;             if (2 * st <= w) {
;                 const bf16x8 bfr = __builtin_bit_cast(bf16x8, (u32x4){sfr[st][0], sfr[st][1], sfr[st][2], sfr[st][3]});
; #pragma unroll
;                 for (int vb = 0; vb < 8; ++vb) { const bf16x8 a = tr_frag_V(L + ML_VS, 32 * st + 4 * fq, 32 * st + 16 + 4 * fq, vb, tl); acc[vb] = __builtin_amdgcn_mfma_f32_16x16x32_bf16(a, bfr, acc[vb], 0, 0, 0); }
;             }
;         }
.LBB0_436:
	ds_read_b64_tr_b16 v[240:241], v224 offset:51200
	ds_read_b64_tr_b16 v[242:243], v224 offset:55296
	ds_read_b64_tr_b16 v[244:245], v214 offset:51200
	ds_read_b64_tr_b16 v[246:247], v214 offset:55296
	ds_read_b64_tr_b16 v[248:249], v215 offset:51200
	ds_read_b64_tr_b16 v[250:251], v215 offset:55296
	s_waitcnt lgkmcnt(4)
	v_mfma_f32_16x16x32_bf16 v[70:73], v[240:243], v[54:57], v[70:73]
	ds_read_b64_tr_b16 v[240:241], v216 offset:51200
	ds_read_b64_tr_b16 v[242:243], v216 offset:55296
	s_waitcnt lgkmcnt(4)
	v_mfma_f32_16x16x32_bf16 v[74:77], v[244:247], v[54:57], v[74:77]
	ds_read_b64_tr_b16 v[244:245], v217 offset:51200
	ds_read_b64_tr_b16 v[246:247], v217 offset:55296
	s_waitcnt lgkmcnt(4)
	v_mfma_f32_16x16x32_bf16 v[78:81], v[248:251], v[54:57], v[78:81]
	ds_read_b64_tr_b16 v[248:249], v218 offset:51200
	ds_read_b64_tr_b16 v[250:251], v218 offset:55296
	s_waitcnt lgkmcnt(4)
	v_mfma_f32_16x16x32_bf16 v[82:85], v[240:243], v[54:57], v[82:85]
	ds_read_b64_tr_b16 v[240:241], v219 offset:51200
	ds_read_b64_tr_b16 v[242:243], v219 offset:55296
	s_waitcnt lgkmcnt(4)
	v_mfma_f32_16x16x32_bf16 v[86:89], v[244:247], v[54:57], v[86:89]
	ds_read_b64_tr_b16 v[244:245], v220 offset:51200
	ds_read_b64_tr_b16 v[246:247], v220 offset:55296
	s_waitcnt lgkmcnt(4)
	v_mfma_f32_16x16x32_bf16 v[90:93], v[248:251], v[54:57], v[90:93]
	s_waitcnt lgkmcnt(2)
	v_mfma_f32_16x16x32_bf16 v[94:97], v[240:243], v[54:57], v[94:97]
	s_waitcnt lgkmcnt(0)
	v_mfma_f32_16x16x32_bf16 v[62:65], v[244:247], v[54:57], v[62:65]
	s_and_b64 vcc, exec, s[76:77]
	s_cbranch_vccz .LBB0_400
	s_branch .LBB0_401
